# v5 + int8 GEMM epilogues (P2/P7/P17): the 8 row-scale loads are issued before the K-loop into spare VGPRs, epilogue waits vmcnt(8) instead of draining the next unit's stage loads
# baseline (speedup 1.0000x reference)
.LBB0_243:
	s_ashr_i32 s17, s16, 31
	s_lshl_b64 s[18:19], s[16:17], 19
	s_add_u32 s18, s72, s18
	s_addc_u32 s19, s73, s19
	s_and_b64 s[20:21], s[0:1], exec
	s_cselect_b32 s17, s19, s25
	s_cselect_b32 s47, s18, s24
	s_ashr_i32 s15, s14, 31
	s_lshl_b64 s[20:21], s[14:15], 19
	s_add_u32 s20, s30, s20
	s_addc_u32 s21, s31, s21
	s_and_b64 s[28:29], s[0:1], exec
	s_cselect_b32 s15, s21, s27
	s_cselect_b32 s48, s20, s26
	s_add_u32 s24, s24, 0x40080
	s_addc_u32 s25, s25, 0
	s_add_u32 s49, s26, 0x100
	v_mov_b32_e32 v2, 0
	s_addc_u32 s50, s27, 0
	s_mov_b32 s51, -2
	v_mov_b32_e32 v3, v2
	v_mov_b32_e32 v4, v2
	v_mov_b32_e32 v5, v2
	v_mov_b32_e32 v6, v2
	v_mov_b32_e32 v7, v2
	v_mov_b32_e32 v8, v2
	v_mov_b32_e32 v9, v2
	v_mov_b32_e32 v10, v2
	v_mov_b32_e32 v11, v2
	v_mov_b32_e32 v12, v2
	v_mov_b32_e32 v13, v2
	v_mov_b32_e32 v18, v2
	v_mov_b32_e32 v19, v2
	v_mov_b32_e32 v20, v2
	v_mov_b32_e32 v21, v2
	v_mov_b32_e32 v26, v2
	v_mov_b32_e32 v27, v2
	v_mov_b32_e32 v28, v2
	v_mov_b32_e32 v29, v2
	v_mov_b32_e32 v34, v2
	v_mov_b32_e32 v35, v2
	v_mov_b32_e32 v36, v2
	v_mov_b32_e32 v37, v2
	v_mov_b32_e32 v42, v2
	v_mov_b32_e32 v43, v2
	v_mov_b32_e32 v44, v2
	v_mov_b32_e32 v45, v2
	v_mov_b32_e32 v50, v2
	v_mov_b32_e32 v51, v2
	v_mov_b32_e32 v52, v2
	v_mov_b32_e32 v53, v2
	v_mov_b32_e32 v14, v2
	v_mov_b32_e32 v15, v2
	v_mov_b32_e32 v16, v2
	v_mov_b32_e32 v17, v2
	v_mov_b32_e32 v22, v2
	v_mov_b32_e32 v23, v2
	v_mov_b32_e32 v24, v2
	v_mov_b32_e32 v25, v2
	v_mov_b32_e32 v30, v2
	v_mov_b32_e32 v31, v2
	v_mov_b32_e32 v32, v2
	v_mov_b32_e32 v33, v2
	v_mov_b32_e32 v38, v2
	v_mov_b32_e32 v39, v2
	v_mov_b32_e32 v40, v2
	v_mov_b32_e32 v41, v2
	v_mov_b32_e32 v46, v2
	v_mov_b32_e32 v47, v2
	v_mov_b32_e32 v48, v2
	v_mov_b32_e32 v49, v2
	v_mov_b32_e32 v54, v2
	v_mov_b32_e32 v55, v2
	v_mov_b32_e32 v56, v2
	v_mov_b32_e32 v57, v2
	v_mov_b32_e32 v58, v2
	v_mov_b32_e32 v59, v2
	v_mov_b32_e32 v60, v2
	v_mov_b32_e32 v61, v2
	v_mov_b32_e32 v62, v2
	v_mov_b32_e32 v63, v2
	v_mov_b32_e32 v64, v2
	v_mov_b32_e32 v65, v2
	v_mov_b32_e32 v66, v2
	v_mov_b32_e32 v67, v2
	v_mov_b32_e32 v68, v2
	v_mov_b32_e32 v69, v2
	v_mov_b32_e32 v70, v2
	v_mov_b32_e32 v71, v2
	v_mov_b32_e32 v72, v2
	v_mov_b32_e32 v73, v2
	v_mov_b32_e32 v74, v2
	v_mov_b32_e32 v75, v2
	v_mov_b32_e32 v76, v2
	v_mov_b32_e32 v77, v2
	v_mov_b32_e32 v82, v2
	v_mov_b32_e32 v83, v2
	v_mov_b32_e32 v84, v2
	v_mov_b32_e32 v85, v2
	v_mov_b32_e32 v90, v2
	v_mov_b32_e32 v91, v2
	v_mov_b32_e32 v92, v2
	v_mov_b32_e32 v93, v2
	v_mov_b32_e32 v102, v2
	v_mov_b32_e32 v103, v2
	v_mov_b32_e32 v104, v2
	v_mov_b32_e32 v105, v2
	v_mov_b32_e32 v106, v2
	v_mov_b32_e32 v107, v2
	v_mov_b32_e32 v108, v2
	v_mov_b32_e32 v109, v2
	v_mov_b32_e32 v110, v2
	v_mov_b32_e32 v111, v2
	v_mov_b32_e32 v112, v2
	v_mov_b32_e32 v113, v2
	v_mov_b32_e32 v78, v2
	v_mov_b32_e32 v79, v2
	v_mov_b32_e32 v80, v2
	v_mov_b32_e32 v81, v2
	v_mov_b32_e32 v86, v2
	v_mov_b32_e32 v87, v2
	v_mov_b32_e32 v88, v2
	v_mov_b32_e32 v89, v2
	v_mov_b32_e32 v94, v2
	v_mov_b32_e32 v95, v2
	v_mov_b32_e32 v96, v2
	v_mov_b32_e32 v97, v2
	v_mov_b32_e32 v98, v2
	v_mov_b32_e32 v99, v2
	v_mov_b32_e32 v100, v2
	v_mov_b32_e32 v101, v2
	v_mov_b32_e32 v114, v2
	v_mov_b32_e32 v115, v2
	v_mov_b32_e32 v116, v2
	v_mov_b32_e32 v117, v2
	v_mov_b32_e32 v118, v2
	v_mov_b32_e32 v119, v2
	v_mov_b32_e32 v120, v2
	v_mov_b32_e32 v121, v2
	v_mov_b32_e32 v122, v2
	v_mov_b32_e32 v123, v2
	v_mov_b32_e32 v124, v2
	v_mov_b32_e32 v125, v2
	v_mov_b32_e32 v126, v2
	v_mov_b32_e32 v127, v2
	v_mov_b32_e32 v128, v2
	v_mov_b32_e32 v129, v2
	v_lshl_add_u32 v234, s22, 8, v181
	v_ashrrev_i32_e32 v235, 31, v234
	v_lshl_add_u64 v[236:237], v[234:235], 2, s[6:7]
	global_load_dword v240, v[236:237], off
	global_load_dword v241, v[236:237], off offset:64
	global_load_dword v242, v[236:237], off offset:128
	global_load_dword v243, v[236:237], off offset:192
	global_load_dword v244, v[236:237], off offset:512
	global_load_dword v245, v[236:237], off offset:576
	global_load_dword v246, v[236:237], off offset:640
	global_load_dword v247, v[236:237], off offset:704

.LBB0_247:
	v_lshl_add_u32 v130, s22, 8, v181
	v_ashrrev_i32_e32 v131, 31, v130
	v_cvt_f32_i32_e32 v150, v90
	v_add_u32_e32 v90, 0x80, v130
	s_nop 15
	s_nop 15
	v_lshl_add_u64 v[132:133], v[130:131], 2, s[6:7]
	v_cvt_f32_i32_e32 v140, v106
	v_cvt_f32_i32_e32 v146, v102
	v_cvt_f32_i32_e32 v148, v104
	v_cvt_f32_i32_e32 v151, v91
	v_add_u32_e32 v102, 0x90, v130
	v_add_u32_e32 v104, 0xa0, v130
	v_add_u32_e32 v106, 0xb0, v130
	v_ashrrev_i32_e32 v91, 31, v90
	v_mov_b32_e32 v131, v240
	v_mov_b32_e32 v134, v241
	v_cvt_f32_i32_e32 v141, v107
	v_cvt_f32_i32_e32 v142, v108
	v_cvt_f32_i32_e32 v143, v109
	v_cvt_f32_i32_e32 v147, v103
	v_cvt_f32_i32_e32 v149, v105
	v_ashrrev_i32_e32 v103, 31, v102
	v_ashrrev_i32_e32 v105, 31, v104
	v_ashrrev_i32_e32 v107, 31, v106
	v_lshl_add_u64 v[108:109], v[90:91], 2, s[6:7]
	v_mov_b32_e32 v135, v242
	v_cvt_f32_i32_e32 v136, v110
	v_cvt_f32_i32_e32 v137, v111
	v_cvt_f32_i32_e32 v138, v112
	v_cvt_f32_i32_e32 v139, v113
	v_cvt_f32_i32_e32 v144, v114
	v_cvt_f32_i32_e32 v145, v115
	v_mov_b32_e32 v132, v243
	v_lshl_add_u64 v[110:111], v[102:103], 2, s[6:7]
	v_lshl_add_u64 v[112:113], v[104:105], 2, s[6:7]
	v_lshl_add_u64 v[114:115], v[106:107], 2, s[6:7]
	v_mov_b32_e32 v91, v244
	v_mov_b32_e32 v103, v245
	v_mov_b32_e32 v105, v246
	v_mov_b32_e32 v107, v247
	v_cvt_f32_i32_e32 v62, v62
	v_cvt_f32_i32_e32 v63, v63
	v_cvt_f32_i32_e32 v64, v64
	v_cvt_f32_i32_e32 v65, v65
	v_cvt_f32_i32_e32 v58, v58
	v_cvt_f32_i32_e32 v59, v59
	v_cvt_f32_i32_e32 v60, v60
	v_cvt_f32_i32_e32 v61, v61
	v_cvt_f32_i32_e32 v50, v50
	v_cvt_f32_i32_e32 v51, v51
	v_cvt_f32_i32_e32 v52, v52
	v_cvt_f32_i32_e32 v53, v53
	v_cvt_f32_i32_e32 v42, v42
	v_cvt_f32_i32_e32 v43, v43
	v_cvt_f32_i32_e32 v44, v44
	v_cvt_f32_i32_e32 v45, v45
	v_cvt_f32_i32_e32 v54, v54
	v_cvt_f32_i32_e32 v55, v55
	v_cvt_f32_i32_e32 v56, v56
	v_cvt_f32_i32_e32 v57, v57
	v_cvt_f32_i32_e32 v46, v46
	v_cvt_f32_i32_e32 v47, v47
	v_cvt_f32_i32_e32 v48, v48
	v_cvt_f32_i32_e32 v49, v49
	v_cvt_f32_i32_e32 v34, v34
	v_cvt_f32_i32_e32 v35, v35
	v_cvt_f32_i32_e32 v36, v36
	v_cvt_f32_i32_e32 v37, v37
	v_cvt_f32_i32_e32 v26, v26
	v_cvt_f32_i32_e32 v27, v27
	v_cvt_f32_i32_e32 v28, v28
	v_cvt_f32_i32_e32 v29, v29
	v_cvt_f32_i32_e32 v126, v126
	v_cvt_f32_i32_e32 v127, v127
	v_cvt_f32_i32_e32 v128, v128
	v_cvt_f32_i32_e32 v129, v129
	v_cvt_f32_i32_e32 v122, v122
	v_cvt_f32_i32_e32 v123, v123
	v_cvt_f32_i32_e32 v124, v124
	v_cvt_f32_i32_e32 v125, v125
	v_cvt_f32_i32_e32 v118, v118
	v_cvt_f32_i32_e32 v119, v119
	v_cvt_f32_i32_e32 v120, v120
	v_cvt_f32_i32_e32 v121, v121
	v_cvt_f32_i32_e32 v116, v116
	v_cvt_f32_i32_e32 v117, v117
	v_cvt_f32_i32_e32 v92, v92
	v_cvt_f32_i32_e32 v93, v93
	v_cvt_f32_i32_e32 v38, v38
	v_cvt_f32_i32_e32 v39, v39
	v_cvt_f32_i32_e32 v40, v40
	v_cvt_f32_i32_e32 v41, v41
	v_cvt_f32_i32_e32 v30, v30
	v_cvt_f32_i32_e32 v31, v31
	v_cvt_f32_i32_e32 v32, v32
	v_cvt_f32_i32_e32 v33, v33
	v_cvt_f32_i32_e32 v18, v18
	v_cvt_f32_i32_e32 v19, v19
	v_cvt_f32_i32_e32 v20, v20
	v_cvt_f32_i32_e32 v21, v21
	v_cvt_f32_i32_e32 v10, v10
	v_cvt_f32_i32_e32 v11, v11
	v_cvt_f32_i32_e32 v12, v12
	v_cvt_f32_i32_e32 v13, v13
	v_cvt_f32_i32_e32 v98, v98
	v_cvt_f32_i32_e32 v99, v99
	v_cvt_f32_i32_e32 v100, v100
	v_cvt_f32_i32_e32 v101, v101
	v_cvt_f32_i32_e32 v94, v94
	v_cvt_f32_i32_e32 v95, v95
	v_cvt_f32_i32_e32 v96, v96
	v_cvt_f32_i32_e32 v97, v97
	v_cvt_f32_i32_e32 v82, v82
	v_cvt_f32_i32_e32 v83, v83
	v_cvt_f32_i32_e32 v84, v84
	v_cvt_f32_i32_e32 v85, v85
	v_cvt_f32_i32_e32 v74, v74
	v_cvt_f32_i32_e32 v75, v75
	v_cvt_f32_i32_e32 v76, v76
	v_cvt_f32_i32_e32 v77, v77
	s_waitcnt vmcnt(8)
	v_mul_f32_e32 v91, v1, v91
	v_cvt_f32_i32_e32 v2, v2
	v_mul_f32_e32 v62, v91, v62
	v_mul_f32_e32 v63, v91, v63
	v_mul_f32_e32 v64, v91, v64
	v_mul_f32_e32 v65, v91, v65
	v_mul_f32_e32 v58, v91, v58
	v_mul_f32_e32 v59, v91, v59
	v_mul_f32_e32 v60, v91, v60
	v_mul_f32_e32 v61, v91, v61
	v_mul_f32_e32 v50, v91, v50
	v_mul_f32_e32 v51, v91, v51
	v_mul_f32_e32 v52, v91, v52
	v_mul_f32_e32 v53, v91, v53
	v_mul_f32_e32 v42, v91, v42
	v_mul_f32_e32 v43, v91, v43
	v_mul_f32_e32 v44, v91, v44
	v_mul_f32_e32 v45, v91, v45
	v_mul_f32_e32 v91, v1, v103
	v_cvt_f32_i32_e32 v3, v3
	v_mul_f32_e32 v108, v1, v131
	v_mul_f32_e32 v109, v1, v134
	v_mul_f32_e32 v54, v91, v54
	v_mul_f32_e32 v55, v91, v55
	v_mul_f32_e32 v56, v91, v56
	v_mul_f32_e32 v57, v91, v57
	v_mul_f32_e32 v46, v91, v46
	v_mul_f32_e32 v47, v91, v47
	v_mul_f32_e32 v48, v91, v48
	v_mul_f32_e32 v49, v91, v49
	v_mul_f32_e32 v34, v91, v34
	v_mul_f32_e32 v35, v91, v35
	v_mul_f32_e32 v36, v91, v36
	v_mul_f32_e32 v37, v91, v37
	v_mul_f32_e32 v26, v91, v26
	v_mul_f32_e32 v27, v91, v27
	v_mul_f32_e32 v28, v91, v28
	v_mul_f32_e32 v29, v91, v29
	v_mul_f32_e32 v91, v1, v105
	v_cvt_f32_i32_e32 v6, v6
	v_cvt_f32_i32_e32 v7, v7
	v_mul_f32_e32 v110, v108, v126
	v_mul_f32_e32 v111, v108, v127
	v_mul_f32_e32 v112, v108, v128
	v_mul_f32_e32 v113, v108, v129
	v_mul_f32_e32 v114, v108, v122
	v_mul_f32_e32 v115, v108, v123
	v_mul_f32_e32 v122, v108, v124
	v_mul_f32_e32 v123, v108, v125
	v_mul_f32_e32 v124, v108, v136
	v_mul_f32_e32 v125, v108, v137
	v_mul_f32_e32 v126, v108, v138
	v_mul_f32_e32 v127, v108, v139
	v_mul_f32_e32 v128, v108, v140
	v_mul_f32_e32 v129, v108, v141
	v_mul_f32_e32 v118, v109, v118
	v_mul_f32_e32 v119, v109, v119
	v_mul_f32_e32 v120, v109, v120
	v_mul_f32_e32 v121, v109, v121
	v_mul_f32_e32 v133, v109, v144
	v_mul_f32_e32 v134, v109, v145
	v_mul_f32_e32 v116, v109, v116
	v_mul_f32_e32 v117, v109, v117
	v_mul_f32_e32 v136, v109, v146
	v_mul_f32_e32 v137, v109, v147
	v_mul_f32_e32 v138, v109, v148
	v_mul_f32_e32 v139, v109, v149
	v_mul_f32_e32 v140, v109, v150
	v_mul_f32_e32 v141, v109, v151
	v_mul_f32_e32 v92, v109, v92
	v_mul_f32_e32 v93, v109, v93
	v_mul_f32_e32 v109, v1, v135
	v_cvt_f32_i32_e32 v86, v86
	v_cvt_f32_i32_e32 v87, v87
	v_cvt_f32_i32_e32 v88, v88
	v_cvt_f32_i32_e32 v89, v89
	v_cvt_f32_i32_e32 v78, v78
	v_cvt_f32_i32_e32 v79, v79
	v_cvt_f32_i32_e32 v80, v80
	v_cvt_f32_i32_e32 v81, v81
	v_cvt_f32_i32_e32 v70, v70
	v_cvt_f32_i32_e32 v71, v71
	v_cvt_f32_i32_e32 v72, v72
	v_cvt_f32_i32_e32 v73, v73
	v_cvt_f32_i32_e32 v66, v66
	v_cvt_f32_i32_e32 v67, v67
	v_cvt_f32_i32_e32 v68, v68
	v_cvt_f32_i32_e32 v69, v69
	v_mul_f32_e32 v38, v91, v38
	v_mul_f32_e32 v39, v91, v39
	v_mul_f32_e32 v40, v91, v40
	v_mul_f32_e32 v41, v91, v41
	v_mul_f32_e32 v30, v91, v30
	v_mul_f32_e32 v31, v91, v31
	v_mul_f32_e32 v32, v91, v32
	v_mul_f32_e32 v33, v91, v33
	v_mul_f32_e32 v18, v91, v18
	v_mul_f32_e32 v19, v91, v19
	v_mul_f32_e32 v20, v91, v20
	v_mul_f32_e32 v21, v91, v21
	v_mul_f32_e32 v10, v91, v10
	v_mul_f32_e32 v11, v91, v11
	v_mul_f32_e32 v12, v91, v12
	v_mul_f32_e32 v13, v91, v13
	v_mul_f32_e32 v91, v1, v107
	v_cvt_f32_i32_e32 v8, v8
	v_cvt_f32_i32_e32 v9, v9
	v_mul_f32_e32 v98, v109, v98
	v_mul_f32_e32 v99, v109, v99
	v_mul_f32_e32 v100, v109, v100
	v_mul_f32_e32 v101, v109, v101
	v_mul_f32_e32 v94, v109, v94
	v_mul_f32_e32 v95, v109, v95
	v_mul_f32_e32 v96, v109, v96
	v_mul_f32_e32 v97, v109, v97
	v_mul_f32_e32 v82, v109, v82
	v_mul_f32_e32 v83, v109, v83
	v_mul_f32_e32 v84, v109, v84
	v_mul_f32_e32 v85, v109, v85
	v_mul_f32_e32 v74, v109, v74
	v_mul_f32_e32 v75, v109, v75
	v_mul_f32_e32 v76, v109, v76
	v_mul_f32_e32 v77, v109, v77
	v_mul_f32_e32 v109, v1, v132
	v_cvt_f32_i32_e32 v22, v22
	v_cvt_f32_i32_e32 v23, v23
	v_cvt_f32_i32_e32 v24, v24
	v_cvt_f32_i32_e32 v25, v25
	v_cvt_f32_i32_e32 v14, v14
	v_cvt_f32_i32_e32 v15, v15
	v_cvt_f32_i32_e32 v16, v16
	v_cvt_f32_i32_e32 v17, v17
	v_cvt_f32_i32_e32 v4, v4
	v_cvt_f32_i32_e32 v5, v5
	v_mul_f32_e32 v132, v91, v2
	v_lshl_or_b32 v2, s46, 8, v191
	v_mul_f32_e32 v135, v91, v3
	v_ashrrev_i32_e32 v3, 31, v2
	v_mul_f32_e32 v103, v91, v6
	v_mul_f32_e32 v105, v91, v7
	v_lshl_add_u64 v[6:7], v[2:3], 1, s[8:9]
	v_mul_f32_e32 v86, v109, v86
	v_mul_f32_e32 v87, v109, v87
	v_mul_f32_e32 v88, v109, v88
	v_mul_f32_e32 v89, v109, v89
	v_mul_f32_e32 v78, v109, v78
	v_mul_f32_e32 v79, v109, v79
	v_mul_f32_e32 v80, v109, v80
	v_mul_f32_e32 v81, v109, v81
	v_mul_f32_e32 v70, v109, v70
	v_mul_f32_e32 v71, v109, v71
	v_mul_f32_e32 v72, v109, v72
	v_mul_f32_e32 v73, v109, v73
	v_mul_f32_e32 v66, v109, v66
	v_mul_f32_e32 v67, v109, v67
	v_mul_f32_e32 v68, v109, v68
	v_mul_f32_e32 v69, v109, v69
	v_mul_f32_e32 v107, v91, v8
	v_mul_f32_e32 v109, v91, v9
	v_mad_i64_i32 v[8:9], s[24:25], v130, s45, v[6:7]
	v_cvt_pk_bf16_f32 v2, v110, v111
	v_mul_f32_e32 v131, v108, v142
	v_mul_f32_e32 v22, v91, v22
	v_mul_f32_e32 v23, v91, v23
	v_mul_f32_e32 v24, v91, v24
	v_mul_f32_e32 v25, v91, v25
	v_mul_f32_e32 v14, v91, v14
	v_mul_f32_e32 v15, v91, v15
	v_mul_f32_e32 v16, v91, v16
	v_mul_f32_e32 v17, v91, v17
	v_mul_f32_e32 v142, v91, v4
	v_mul_f32_e32 v91, v91, v5
	v_cvt_pk_bf16_f32 v3, v112, v113
	v_cvt_pk_bf16_f32 v4, v114, v115
	v_cvt_pk_bf16_f32 v5, v122, v123
	global_store_dwordx4 v[8:9], v[2:5], off
	v_mul_f32_e32 v108, v108, v143
	v_readlane_b32 s48, v250, 56
	v_cvt_pk_bf16_f32 v2, v124, v125
	v_cvt_pk_bf16_f32 v3, v126, v127
	v_cvt_pk_bf16_f32 v4, v128, v129
	v_cvt_pk_bf16_f32 v5, v131, v108
	global_store_dwordx4 v[8:9], v[2:5], off offset:256
	s_andn2_b64 vcc, exec, s[0:1]
	s_mov_b64 s[0:1], -1
	v_or_b32_e32 v2, 16, v130
	v_mad_i64_i32 v[8:9], s[24:25], v2, s45, v[6:7]
	v_cvt_pk_bf16_f32 v2, v118, v119
	v_cvt_pk_bf16_f32 v3, v120, v121
	v_cvt_pk_bf16_f32 v4, v133, v134
	v_cvt_pk_bf16_f32 v5, v116, v117
	global_store_dwordx4 v[8:9], v[2:5], off
	v_readlane_b32 s60, v251, 4
	v_readlane_b32 s61, v251, 5
	v_cvt_pk_bf16_f32 v2, v136, v137
	v_cvt_pk_bf16_f32 v3, v138, v139
	v_cvt_pk_bf16_f32 v4, v140, v141
	v_cvt_pk_bf16_f32 v5, v92, v93
	global_store_dwordx4 v[8:9], v[2:5], off offset:256
	v_readlane_b32 s62, v251, 6
	v_readlane_b32 s63, v251, 7
	v_or_b32_e32 v2, 32, v130
	v_mad_i64_i32 v[8:9], s[24:25], v2, s45, v[6:7]
	v_cvt_pk_bf16_f32 v2, v98, v99
	v_cvt_pk_bf16_f32 v3, v100, v101
	v_cvt_pk_bf16_f32 v4, v94, v95
	v_cvt_pk_bf16_f32 v5, v96, v97
	global_store_dwordx4 v[8:9], v[2:5], off
	v_readlane_b32 s49, v250, 57
	v_readlane_b32 s50, v250, 58
	v_cvt_pk_bf16_f32 v2, v82, v83
	v_cvt_pk_bf16_f32 v3, v84, v85
	v_cvt_pk_bf16_f32 v4, v74, v75
	v_cvt_pk_bf16_f32 v5, v76, v77
	global_store_dwordx4 v[8:9], v[2:5], off offset:256
	v_readlane_b32 s51, v250, 59
	v_readlane_b32 s52, v250, 60
	v_or_b32_e32 v2, 48, v130
	v_mad_i64_i32 v[8:9], s[24:25], v2, s45, v[6:7]
	v_cvt_pk_bf16_f32 v2, v86, v87
	v_cvt_pk_bf16_f32 v3, v88, v89
	v_cvt_pk_bf16_f32 v4, v78, v79
	v_cvt_pk_bf16_f32 v5, v80, v81
	global_store_dwordx4 v[8:9], v[2:5], off
	v_readlane_b32 s53, v250, 61
	v_readlane_b32 s54, v250, 62
	v_cvt_pk_bf16_f32 v2, v70, v71
	v_cvt_pk_bf16_f32 v3, v72, v73
	v_cvt_pk_bf16_f32 v4, v66, v67
	v_cvt_pk_bf16_f32 v5, v68, v69
	global_store_dwordx4 v[8:9], v[2:5], off offset:256
	v_mad_i64_i32 v[8:9], s[24:25], v90, s45, v[6:7]
	s_nop 0
	v_cvt_pk_bf16_f32 v2, v62, v63
	v_cvt_pk_bf16_f32 v3, v64, v65
	v_cvt_pk_bf16_f32 v4, v58, v59
	v_cvt_pk_bf16_f32 v5, v60, v61
	global_store_dwordx4 v[8:9], v[2:5], off
	v_readlane_b32 s55, v250, 63
	v_readlane_b32 s56, v251, 0
	v_cvt_pk_bf16_f32 v2, v50, v51
	v_cvt_pk_bf16_f32 v3, v52, v53
	v_cvt_pk_bf16_f32 v4, v42, v43
	v_cvt_pk_bf16_f32 v5, v44, v45
	global_store_dwordx4 v[8:9], v[2:5], off offset:256
	v_mad_i64_i32 v[8:9], s[24:25], v102, s45, v[6:7]
	s_nop 0
	v_cvt_pk_bf16_f32 v2, v54, v55
	v_cvt_pk_bf16_f32 v3, v56, v57
	v_cvt_pk_bf16_f32 v4, v46, v47
	v_cvt_pk_bf16_f32 v5, v48, v49
	global_store_dwordx4 v[8:9], v[2:5], off
	v_readlane_b32 s57, v251, 1
	v_readlane_b32 s58, v251, 2
	v_cvt_pk_bf16_f32 v2, v34, v35
	v_cvt_pk_bf16_f32 v3, v36, v37
	v_cvt_pk_bf16_f32 v4, v26, v27
	v_cvt_pk_bf16_f32 v5, v28, v29
	global_store_dwordx4 v[8:9], v[2:5], off offset:256
	v_mad_i64_i32 v[8:9], s[24:25], v104, s45, v[6:7]
	s_nop 0
	v_cvt_pk_bf16_f32 v2, v38, v39
	v_cvt_pk_bf16_f32 v3, v40, v41
	v_cvt_pk_bf16_f32 v4, v30, v31
	v_cvt_pk_bf16_f32 v5, v32, v33
	global_store_dwordx4 v[8:9], v[2:5], off
	v_mad_i64_i32 v[6:7], s[24:25], v106, s45, v[6:7]
	s_nop 0
	v_cvt_pk_bf16_f32 v2, v18, v19
	v_cvt_pk_bf16_f32 v3, v20, v21
	v_cvt_pk_bf16_f32 v4, v10, v11
	v_cvt_pk_bf16_f32 v5, v12, v13
	global_store_dwordx4 v[8:9], v[2:5], off offset:256
	v_readlane_b32 s59, v251, 3
	s_nop 0
	v_cvt_pk_bf16_f32 v2, v22, v23
	v_cvt_pk_bf16_f32 v3, v24, v25
	v_cvt_pk_bf16_f32 v4, v14, v15
	v_cvt_pk_bf16_f32 v5, v16, v17
	global_store_dwordx4 v[6:7], v[2:5], off
	s_nop 1
	v_cvt_pk_bf16_f32 v2, v103, v105
	v_cvt_pk_bf16_f32 v3, v107, v109
	v_cvt_pk_bf16_f32 v4, v132, v135
	v_cvt_pk_bf16_f32 v5, v142, v91
	global_store_dwordx4 v[6:7], v[2:5], off offset:256
	s_cbranch_vccnz .LBB0_240
	s_andn2_b64 vcc, exec, s[4:5]
	s_cbranch_vccnz .LBB0_239
	s_barrier
	s_branch .LBB0_239

.LBB0_763:
	s_ashr_i32 s17, s16, 31
	s_lshl_b64 s[18:19], s[16:17], 19
	s_add_u32 s18, s72, s18
	s_addc_u32 s19, s73, s19
	s_and_b64 s[20:21], s[0:1], exec
	s_cselect_b32 s17, s19, s25
	s_cselect_b32 s47, s18, s24
	s_ashr_i32 s15, s14, 31
	s_lshl_b64 s[20:21], s[14:15], 19
	s_add_u32 s20, s30, s20
	s_addc_u32 s21, s31, s21
	s_and_b64 s[28:29], s[0:1], exec
	s_cselect_b32 s15, s21, s27
	s_cselect_b32 s48, s20, s26
	s_add_u32 s24, s24, 0x40080
	s_addc_u32 s25, s25, 0
	s_add_u32 s49, s26, 0x100
	v_mov_b32_e32 v2, 0
	s_addc_u32 s50, s27, 0
	s_mov_b32 s51, -2
	v_mov_b32_e32 v3, v2
	v_mov_b32_e32 v4, v2
	v_mov_b32_e32 v5, v2
	v_mov_b32_e32 v6, v2
	v_mov_b32_e32 v7, v2
	v_mov_b32_e32 v8, v2
	v_mov_b32_e32 v9, v2
	v_mov_b32_e32 v14, v2
	v_mov_b32_e32 v15, v2
	v_mov_b32_e32 v16, v2
	v_mov_b32_e32 v17, v2
	s_waitcnt vmcnt(0)
	v_mov_b32_e32 v22, v2
	v_mov_b32_e32 v23, v2
	v_mov_b32_e32 v24, v2
	v_mov_b32_e32 v25, v2
	v_mov_b32_e32 v30, v2
	v_mov_b32_e32 v31, v2
	v_mov_b32_e32 v32, v2
	v_mov_b32_e32 v33, v2
	v_mov_b32_e32 v38, v2
	v_mov_b32_e32 v39, v2
	v_mov_b32_e32 v40, v2
	v_mov_b32_e32 v41, v2
	v_mov_b32_e32 v46, v2
	v_mov_b32_e32 v47, v2
	v_mov_b32_e32 v48, v2
	v_mov_b32_e32 v49, v2
	v_mov_b32_e32 v54, v2
	v_mov_b32_e32 v55, v2
	v_mov_b32_e32 v56, v2
	v_mov_b32_e32 v57, v2
	v_mov_b32_e32 v10, v2
	v_mov_b32_e32 v11, v2
	v_mov_b32_e32 v12, v2
	v_mov_b32_e32 v13, v2
	v_mov_b32_e32 v18, v2
	v_mov_b32_e32 v19, v2
	v_mov_b32_e32 v20, v2
	v_mov_b32_e32 v21, v2
	v_mov_b32_e32 v26, v2
	v_mov_b32_e32 v27, v2
	v_mov_b32_e32 v28, v2
	v_mov_b32_e32 v29, v2
	v_mov_b32_e32 v34, v2
	v_mov_b32_e32 v35, v2
	v_mov_b32_e32 v36, v2
	v_mov_b32_e32 v37, v2
	v_mov_b32_e32 v42, v2
	v_mov_b32_e32 v43, v2
	v_mov_b32_e32 v44, v2
	v_mov_b32_e32 v45, v2
	v_mov_b32_e32 v50, v2
	v_mov_b32_e32 v51, v2
	v_mov_b32_e32 v52, v2
	v_mov_b32_e32 v53, v2
	v_mov_b32_e32 v58, v2
	v_mov_b32_e32 v59, v2
	v_mov_b32_e32 v60, v2
	v_mov_b32_e32 v61, v2
	v_mov_b32_e32 v62, v2
	v_mov_b32_e32 v63, v2
	v_mov_b32_e32 v64, v2
	v_mov_b32_e32 v65, v2
	v_mov_b32_e32 v66, v2
	v_mov_b32_e32 v67, v2
	v_mov_b32_e32 v68, v2
	v_mov_b32_e32 v69, v2
	v_mov_b32_e32 v70, v2
	v_mov_b32_e32 v71, v2
	v_mov_b32_e32 v72, v2
	v_mov_b32_e32 v73, v2
	v_mov_b32_e32 v78, v2
	v_mov_b32_e32 v79, v2
	v_mov_b32_e32 v80, v2
	v_mov_b32_e32 v81, v2
	v_mov_b32_e32 v90, v2
	v_mov_b32_e32 v91, v2
	v_mov_b32_e32 v92, v2
	v_mov_b32_e32 v93, v2
	v_mov_b32_e32 v98, v2
	v_mov_b32_e32 v99, v2
	v_mov_b32_e32 v100, v2
	v_mov_b32_e32 v101, v2
	v_mov_b32_e32 v102, v2
	v_mov_b32_e32 v103, v2
	v_mov_b32_e32 v104, v2
	v_mov_b32_e32 v105, v2
	v_mov_b32_e32 v106, v2
	v_mov_b32_e32 v107, v2
	v_mov_b32_e32 v108, v2
	v_mov_b32_e32 v109, v2
	v_mov_b32_e32 v122, v2
	v_mov_b32_e32 v123, v2
	v_mov_b32_e32 v124, v2
	v_mov_b32_e32 v125, v2
	v_mov_b32_e32 v74, v2
	v_mov_b32_e32 v75, v2
	v_mov_b32_e32 v76, v2
	v_mov_b32_e32 v77, v2
	v_mov_b32_e32 v82, v2
	v_mov_b32_e32 v83, v2
	v_mov_b32_e32 v84, v2
	v_mov_b32_e32 v85, v2
	v_mov_b32_e32 v86, v2
	v_mov_b32_e32 v87, v2
	v_mov_b32_e32 v88, v2
	v_mov_b32_e32 v89, v2
	v_mov_b32_e32 v94, v2
	v_mov_b32_e32 v95, v2
	v_mov_b32_e32 v96, v2
	v_mov_b32_e32 v97, v2
	v_mov_b32_e32 v110, v2
	v_mov_b32_e32 v111, v2
	v_mov_b32_e32 v112, v2
	v_mov_b32_e32 v113, v2
	v_mov_b32_e32 v114, v2
	v_mov_b32_e32 v115, v2
	v_mov_b32_e32 v116, v2
	v_mov_b32_e32 v117, v2
	v_mov_b32_e32 v118, v2
	v_mov_b32_e32 v119, v2
	v_mov_b32_e32 v120, v2
	v_mov_b32_e32 v121, v2
	v_mov_b32_e32 v126, v2
	v_mov_b32_e32 v127, v2
	v_mov_b32_e32 v128, v2
	v_mov_b32_e32 v129, v2
	v_lshl_add_u32 v234, s22, 8, v181
	v_ashrrev_i32_e32 v235, 31, v234
	v_lshl_add_u64 v[236:237], v[234:235], 2, s[6:7]
	global_load_dword v240, v[236:237], off
	global_load_dword v241, v[236:237], off offset:64
	global_load_dword v242, v[236:237], off offset:128
	global_load_dword v243, v[236:237], off offset:192
	global_load_dword v244, v[236:237], off offset:512
	global_load_dword v245, v[236:237], off offset:576
	global_load_dword v246, v[236:237], off offset:640
	global_load_dword v247, v[236:237], off offset:704

.LBB0_767:
	v_lshl_add_u32 v130, s22, 8, v181
	v_ashrrev_i32_e32 v131, 31, v130
	s_nop 15
	s_nop 15
	v_lshl_add_u64 v[134:135], v[130:131], 2, s[6:7]
	v_mov_b32_e32 v131, v240
	v_mov_b32_e32 v146, v241
	v_mov_b32_e32 v147, v242
	v_mov_b32_e32 v158, v243
	v_cvt_f32_i32_e32 v133, v122
	v_cvt_f32_i32_e32 v122, v127
	v_cvt_f32_i32_e32 v127, v124
	v_cvt_f32_i32_e32 v124, v129
	v_cvt_f32_i32_e32 v129, v106
	v_cvt_f32_i32_e32 v106, v119
	v_cvt_f32_i32_e32 v119, v108
	v_cvt_f32_i32_e32 v108, v121
	v_cvt_f32_i32_e32 v121, v102
	v_cvt_f32_i32_e32 v102, v115
	v_cvt_f32_i32_e32 v115, v104
	v_cvt_f32_i32_e32 v104, v117
	v_cvt_f32_i32_e32 v117, v98
	v_add_u32_e32 v98, 0x80, v130
	v_cvt_f32_i32_e32 v135, v99
	v_ashrrev_i32_e32 v99, 31, v98
	v_cvt_f32_i32_e32 v132, v126
	v_cvt_f32_i32_e32 v126, v128
	v_cvt_f32_i32_e32 v128, v118
	v_cvt_f32_i32_e32 v118, v120
	v_cvt_f32_i32_e32 v120, v114
	v_cvt_f32_i32_e32 v114, v116
	v_cvt_f32_i32_e32 v116, v110
	v_cvt_f32_i32_e32 v134, v111
	v_cvt_f32_i32_e32 v111, v100
	v_cvt_f32_i32_e32 v110, v112
	v_cvt_f32_i32_e32 v100, v113
	v_lshl_add_u64 v[112:113], v[98:99], 2, s[6:7]
	v_mov_b32_e32 v99, v244
	v_cvt_f32_i32_e32 v141, v92
	v_add_u32_e32 v92, 0x90, v130
	v_cvt_f32_i32_e32 v137, v90
	v_cvt_f32_i32_e32 v136, v94
	v_cvt_f32_i32_e32 v143, v93
	v_add_u32_e32 v94, 0xa0, v130
	v_add_u32_e32 v90, 0xb0, v130
	v_ashrrev_i32_e32 v93, 31, v92
	v_cvt_f32_i32_e32 v139, v91
	v_cvt_f32_i32_e32 v138, v95
	v_cvt_f32_i32_e32 v140, v96
	v_cvt_f32_i32_e32 v142, v97
	v_ashrrev_i32_e32 v95, 31, v94
	v_ashrrev_i32_e32 v91, 31, v90
	v_lshl_add_u64 v[96:97], v[92:93], 2, s[6:7]
	v_lshl_add_u64 v[112:113], v[94:95], 2, s[6:7]
	v_lshl_add_u64 v[144:145], v[90:91], 2, s[6:7]
	v_mov_b32_e32 v91, v245
	v_mov_b32_e32 v93, v246
	v_mov_b32_e32 v95, v247
	v_cvt_f32_i32_e32 v123, v123
	v_cvt_f32_i32_e32 v125, v125
	v_cvt_f32_i32_e32 v107, v107
	v_cvt_f32_i32_e32 v109, v109
	v_cvt_f32_i32_e32 v103, v103
	v_cvt_f32_i32_e32 v79, v79
	v_cvt_f32_i32_e32 v81, v81
	v_cvt_f32_i32_e32 v71, v71
	v_cvt_f32_i32_e32 v73, v73
	v_cvt_f32_i32_e32 v67, v67
	v_cvt_f32_i32_e32 v69, v69
	v_cvt_f32_i32_e32 v55, v55
	v_cvt_f32_i32_e32 v57, v57
	v_cvt_f32_i32_e32 v47, v47
	v_cvt_f32_i32_e32 v49, v49
	v_cvt_f32_i32_e32 v39, v39
	v_cvt_f32_i32_e32 v41, v41
	v_cvt_f32_i32_e32 v31, v31
	v_cvt_f32_i32_e32 v33, v33
	v_cvt_f32_i32_e32 v23, v23
	v_cvt_f32_i32_e32 v25, v25
	v_cvt_f32_i32_e32 v15, v15
	v_cvt_f32_i32_e32 v17, v17
	v_cvt_f32_i32_e32 v7, v7
	v_cvt_f32_i32_e32 v9, v9
	v_cvt_f32_i32_e32 v3, v3
	v_cvt_f32_i32_e32 v105, v105
	v_cvt_f32_i32_e32 v101, v101
	s_mul_hi_i32 s15, s46, 0x2e8ba2e9
	s_waitcnt vmcnt(8)
	v_mul_f32_e32 v96, v1, v131
	v_pk_mul_f32 v[132:133], v[96:97], v[132:133] op_sel_hi:[0,1]
	v_pk_mul_f32 v[148:149], v[96:97], v[122:123] op_sel_hi:[0,1]
	v_pk_mul_f32 v[150:151], v[96:97], v[126:127] op_sel_hi:[0,1]
	v_pk_mul_f32 v[152:153], v[96:97], v[124:125] op_sel_hi:[0,1]
	v_pk_mul_f32 v[128:129], v[96:97], v[128:129] op_sel_hi:[0,1]
	v_pk_mul_f32 v[154:155], v[96:97], v[106:107] op_sel_hi:[0,1]
	v_pk_mul_f32 v[156:157], v[96:97], v[118:119] op_sel_hi:[0,1]
	v_pk_mul_f32 v[126:127], v[96:97], v[108:109] op_sel_hi:[0,1]
	v_cvt_f32_i32_e32 v97, v78
	v_cvt_f32_i32_e32 v96, v86
	v_cvt_f32_i32_e32 v78, v87
	v_mul_f32_e32 v144, v1, v146
	v_mul_f32_e32 v146, v1, v147
	v_cvt_f32_i32_e32 v87, v80
	v_cvt_f32_i32_e32 v86, v88
	v_cvt_f32_i32_e32 v80, v89
	v_pk_mul_f32 v[122:123], v[144:145], v[102:103] op_sel_hi:[0,1]
	v_pk_mul_f32 v[102:103], v[146:147], v[96:97] op_sel_hi:[0,1]
	v_pk_mul_f32 v[96:97], v[146:147], v[78:79] op_sel_hi:[0,1]
	v_cvt_f32_i32_e32 v79, v70
	v_cvt_f32_i32_e32 v70, v83
	v_pk_mul_f32 v[124:125], v[144:145], v[120:121] op_sel_hi:[0,1]
	v_pk_mul_f32 v[120:121], v[144:145], v[114:115] op_sel_hi:[0,1]
	v_pk_mul_f32 v[114:115], v[144:145], v[134:135] op_sel_hi:[0,1]
	v_pk_mul_f32 v[88:89], v[146:147], v[86:87] op_sel_hi:[0,1]
	v_pk_mul_f32 v[86:87], v[146:147], v[80:81] op_sel_hi:[0,1]
	v_mul_f32_e32 v134, v1, v158
	v_cvt_f32_i32_e32 v78, v82
	v_cvt_f32_i32_e32 v81, v72
	v_cvt_f32_i32_e32 v72, v85
	v_pk_mul_f32 v[82:83], v[134:135], v[70:71] op_sel_hi:[0,1]
	v_cvt_f32_i32_e32 v71, v66
	v_cvt_f32_i32_e32 v66, v75
	v_cvt_f32_i32_e32 v80, v84
	v_pk_mul_f32 v[84:85], v[134:135], v[78:79] op_sel_hi:[0,1]
	v_pk_mul_f32 v[78:79], v[134:135], v[72:73] op_sel_hi:[0,1]
	v_cvt_f32_i32_e32 v70, v74
	v_cvt_f32_i32_e32 v73, v68
	v_cvt_f32_i32_e32 v72, v76
	v_cvt_f32_i32_e32 v68, v77
	v_pk_mul_f32 v[74:75], v[134:135], v[66:67] op_sel_hi:[0,1]
	v_cvt_f32_i32_e32 v67, v54
	v_cvt_f32_i32_e32 v66, v62
	v_cvt_f32_i32_e32 v54, v63
	v_pk_mul_f32 v[80:81], v[134:135], v[80:81] op_sel_hi:[0,1]
	v_pk_mul_f32 v[76:77], v[134:135], v[70:71] op_sel_hi:[0,1]
	v_pk_mul_f32 v[72:73], v[134:135], v[72:73] op_sel_hi:[0,1]
	v_pk_mul_f32 v[70:71], v[134:135], v[68:69] op_sel_hi:[0,1]
	v_mul_f32_e32 v134, v1, v99
	v_cvt_f32_i32_e32 v63, v56
	v_cvt_f32_i32_e32 v62, v64
	v_cvt_f32_i32_e32 v56, v65
	v_pk_mul_f32 v[68:69], v[134:135], v[66:67] op_sel_hi:[0,1]
	v_pk_mul_f32 v[66:67], v[134:135], v[54:55] op_sel_hi:[0,1]
	v_cvt_f32_i32_e32 v55, v46
	v_cvt_f32_i32_e32 v46, v59
	v_pk_mul_f32 v[64:65], v[134:135], v[62:63] op_sel_hi:[0,1]
	v_pk_mul_f32 v[62:63], v[134:135], v[56:57] op_sel_hi:[0,1]
	v_cvt_f32_i32_e32 v54, v58
	v_cvt_f32_i32_e32 v57, v48
	v_cvt_f32_i32_e32 v56, v60
	v_cvt_f32_i32_e32 v48, v61
	v_pk_mul_f32 v[58:59], v[134:135], v[46:47] op_sel_hi:[0,1]
	v_cvt_f32_i32_e32 v47, v38
	v_cvt_f32_i32_e32 v38, v51
	v_pk_mul_f32 v[60:61], v[134:135], v[54:55] op_sel_hi:[0,1]
	v_pk_mul_f32 v[56:57], v[134:135], v[56:57] op_sel_hi:[0,1]
	v_pk_mul_f32 v[54:55], v[134:135], v[48:49] op_sel_hi:[0,1]
	v_mul_f32_e32 v134, v1, v91
	v_cvt_f32_i32_e32 v46, v50
	v_cvt_f32_i32_e32 v49, v40
	v_cvt_f32_i32_e32 v40, v53
	v_pk_mul_f32 v[50:51], v[134:135], v[38:39] op_sel_hi:[0,1]
	v_cvt_f32_i32_e32 v39, v30
	v_cvt_f32_i32_e32 v30, v43
	v_cvt_f32_i32_e32 v48, v52
	v_pk_mul_f32 v[52:53], v[134:135], v[46:47] op_sel_hi:[0,1]
	v_pk_mul_f32 v[46:47], v[134:135], v[40:41] op_sel_hi:[0,1]
	v_cvt_f32_i32_e32 v38, v42
	v_cvt_f32_i32_e32 v41, v32
	v_cvt_f32_i32_e32 v40, v44
	v_cvt_f32_i32_e32 v32, v45
	v_pk_mul_f32 v[42:43], v[134:135], v[30:31] op_sel_hi:[0,1]
	v_cvt_f32_i32_e32 v31, v22
	v_cvt_f32_i32_e32 v22, v35
	v_pk_mul_f32 v[48:49], v[134:135], v[48:49] op_sel_hi:[0,1]
	v_pk_mul_f32 v[44:45], v[134:135], v[38:39] op_sel_hi:[0,1]
	v_pk_mul_f32 v[40:41], v[134:135], v[40:41] op_sel_hi:[0,1]
	v_pk_mul_f32 v[38:39], v[134:135], v[32:33] op_sel_hi:[0,1]
	v_mul_f32_e32 v134, v1, v93
	v_cvt_f32_i32_e32 v30, v34
	v_cvt_f32_i32_e32 v33, v24
	v_cvt_f32_i32_e32 v24, v37
	v_pk_mul_f32 v[34:35], v[134:135], v[22:23] op_sel_hi:[0,1]
	v_cvt_f32_i32_e32 v23, v14
	v_cvt_f32_i32_e32 v14, v27
	v_cvt_f32_i32_e32 v32, v36
	v_pk_mul_f32 v[36:37], v[134:135], v[30:31] op_sel_hi:[0,1]
	v_pk_mul_f32 v[30:31], v[134:135], v[24:25] op_sel_hi:[0,1]
	v_cvt_f32_i32_e32 v22, v26
	v_cvt_f32_i32_e32 v25, v16
	v_cvt_f32_i32_e32 v24, v28
	v_cvt_f32_i32_e32 v16, v29
	v_pk_mul_f32 v[26:27], v[134:135], v[14:15] op_sel_hi:[0,1]
	v_cvt_f32_i32_e32 v15, v6
	v_cvt_f32_i32_e32 v6, v19
	v_pk_mul_f32 v[32:33], v[134:135], v[32:33] op_sel_hi:[0,1]
	v_pk_mul_f32 v[28:29], v[134:135], v[22:23] op_sel_hi:[0,1]
	v_pk_mul_f32 v[24:25], v[134:135], v[24:25] op_sel_hi:[0,1]
	v_pk_mul_f32 v[22:23], v[134:135], v[16:17] op_sel_hi:[0,1]
	v_mul_f32_e32 v134, v1, v95
	v_cvt_f32_i32_e32 v14, v18
	v_cvt_f32_i32_e32 v19, v8
	v_cvt_f32_i32_e32 v18, v20
	v_pk_mul_f32 v[16:17], v[134:135], v[6:7] op_sel_hi:[0,1]
	v_cvt_f32_i32_e32 v7, v2
	v_cvt_f32_i32_e32 v6, v10
	v_cvt_f32_i32_e32 v8, v21
	v_pk_mul_f32 v[20:21], v[134:135], v[14:15] op_sel_hi:[0,1]
	v_pk_mul_f32 v[14:15], v[134:135], v[18:19] op_sel_hi:[0,1]
	v_pk_mul_f32 v[18:19], v[134:135], v[6:7] op_sel_hi:[0,1]
	v_mul_f32_e32 v6, 0xbfb8aa3b, v132
	v_pk_mul_f32 v[108:109], v[146:147], v[136:137] op_sel_hi:[0,1]
	v_cvt_f32_i32_e32 v136, v12
	v_exp_f32_e32 v12, v6
	v_mul_f32_e32 v95, v132, v133
	v_mul_f32_e32 v131, 0xbfb8aa3b, v152
	v_mul_f32_e32 v132, 0xbfb8aa3b, v128
	v_add_f32_e32 v12, 1.0, v12
	v_rcp_f32_e32 v91, v12
	v_mul_f32_e32 v12, 0xbfb8aa3b, v148
	v_exp_f32_e32 v93, v12
	v_exp_f32_e32 v131, v131
	v_mul_f32_e32 v91, v95, v91
	v_mul_f32_e32 v95, 0xbfb8aa3b, v150
	v_exp_f32_e32 v95, v95
	v_add_f32_e32 v93, 1.0, v93
	v_rcp_f32_e32 v93, v93
	v_exp_f32_e32 v132, v132
	v_add_f32_e32 v95, 1.0, v95
	v_rcp_f32_e32 v95, v95
	v_mul_f32_e32 v99, v148, v149
	v_mul_f32_e32 v93, v99, v93
	v_mul_f32_e32 v99, v150, v151
	v_mul_f32_e32 v95, v99, v95
	v_add_f32_e32 v99, 1.0, v131
	v_add_f32_e32 v131, 1.0, v132
	v_rcp_f32_e32 v131, v131
	v_mul_f32_e32 v128, v128, v129
	v_mul_f32_e32 v129, 0xbfb8aa3b, v156
	v_exp_f32_e32 v129, v129
	v_mul_f32_e32 v131, v128, v131
	v_mul_f32_e32 v128, 0xbfb8aa3b, v154
	v_exp_f32_e32 v128, v128
	v_rcp_f32_e32 v99, v99
	v_add_f32_e32 v129, 1.0, v129
	v_mul_f32_e32 v133, 0xbfb8aa3b, v126
	v_add_f32_e32 v128, 1.0, v128
	v_rcp_f32_e32 v128, v128
	v_pk_mul_f32 v[106:107], v[146:147], v[138:139] op_sel_hi:[0,1]
	v_cvt_f32_i32_e32 v2, v11
	v_cvt_f32_i32_e32 v137, v4
	v_cvt_f32_i32_e32 v139, v5
	v_cvt_f32_i32_e32 v138, v13
	v_rcp_f32_e32 v129, v129
	v_exp_f32_e32 v133, v133
	v_mul_f32_e32 v132, v152, v153
	v_mul_f32_e32 v99, v132, v99
	v_mul_f32_e32 v132, v154, v155
	v_mul_f32_e32 v132, v132, v128
	v_mul_f32_e32 v128, v156, v157
	v_pk_mul_f32 v[8:9], v[134:135], v[8:9] op_sel_hi:[0,1]
	v_pk_mul_f32 v[10:11], v[134:135], v[2:3] op_sel_hi:[0,1]
	v_pk_mul_f32 v[4:5], v[134:135], v[136:137] op_sel_hi:[0,1]
	v_pk_mul_f32 v[2:3], v[134:135], v[138:139] op_sel_hi:[0,1]
	v_mul_f32_e32 v134, v128, v129
	v_add_f32_e32 v128, 1.0, v133
	v_rcp_f32_e32 v133, v128
	v_mov_b32_e32 v129, 0
	v_cvt_pk_fp8_f32 v129, v131, v132
	v_mov_b32_e32 v128, 0
	v_cvt_pk_fp8_f32 v128, v91, v93
	v_mul_f32_e32 v91, v126, v127
	v_mul_f32_e32 v91, v91, v133
	v_cvt_pk_fp8_f32 v129, v134, v91 op_sel:[0,0,1]
	v_mul_f32_e32 v91, 0xbfb8aa3b, v124
	v_exp_f32_e32 v91, v91
	v_mul_f32_e32 v93, 0xbfb8aa3b, v122
	v_exp_f32_e32 v93, v93
	v_cvt_pk_fp8_f32 v128, v95, v99 op_sel:[0,0,1]
	v_add_f32_e32 v91, 1.0, v91
	v_rcp_f32_e32 v91, v91
	v_mul_f32_e32 v99, v124, v125
	v_add_f32_e32 v93, 1.0, v93
	v_rcp_f32_e32 v93, v93
	v_mul_f32_e32 v91, v99, v91
	v_mul_f32_e32 v99, 0xbfb8aa3b, v120
	v_exp_f32_e32 v99, v99
	v_pk_mul_f32 v[118:119], v[144:145], v[104:105] op_sel_hi:[0,1]
	v_pk_mul_f32 v[116:117], v[144:145], v[116:117] op_sel_hi:[0,1]
	v_pk_mul_f32 v[112:113], v[144:145], v[110:111] op_sel_hi:[0,1]
	v_mul_f32_e32 v122, v122, v123
	v_mul_f32_e32 v93, v122, v93
	v_mul_f32_e32 v120, v120, v121
	v_mul_f32_e32 v121, 0xbfb8aa3b, v118
	v_mul_f32_e32 v122, 0xbfb8aa3b, v116
	v_mul_f32_e32 v118, v118, v119
	v_mul_f32_e32 v116, v116, v117
	v_mul_f32_e32 v117, 0xbfb8aa3b, v114
	v_mul_f32_e32 v119, 0xbfb8aa3b, v112
	v_add_f32_e32 v99, 1.0, v99
	v_exp_f32_e32 v117, v117
	v_exp_f32_e32 v119, v119
	v_rcp_f32_e32 v99, v99
	v_exp_f32_e32 v121, v121
	v_exp_f32_e32 v122, v122
	v_pk_mul_f32 v[110:111], v[144:145], v[100:101] op_sel_hi:[0,1]
	v_mul_f32_e32 v114, v114, v115
	v_add_f32_e32 v115, 1.0, v117
	v_add_f32_e32 v117, 1.0, v119
	v_mul_f32_e32 v119, 0xbfb8aa3b, v110
	v_mul_f32_e32 v99, v120, v99
	v_add_f32_e32 v120, 1.0, v121
	v_add_f32_e32 v121, 1.0, v122
	v_rcp_f32_e32 v115, v115
	v_rcp_f32_e32 v117, v117
	v_exp_f32_e32 v119, v119
	v_rcp_f32_e32 v121, v121
	v_mul_f32_e32 v112, v112, v113
	v_mul_f32_e32 v114, v114, v115
	v_mul_f32_e32 v115, v112, v117
	v_add_f32_e32 v112, 1.0, v119
	v_mul_f32_e32 v116, v116, v121
	v_rcp_f32_e32 v117, v112
	v_mov_b32_e32 v113, 0
	v_cvt_pk_fp8_f32 v113, v116, v114
	v_mov_b32_e32 v112, 0
	v_cvt_pk_fp8_f32 v112, v91, v93
	v_mul_f32_e32 v91, v110, v111
	v_mul_f32_e32 v91, v91, v117
	v_cvt_pk_fp8_f32 v113, v115, v91 op_sel:[0,0,1]
	v_mul_f32_e32 v91, 0xbfb8aa3b, v108
	v_exp_f32_e32 v91, v91
	v_rcp_f32_e32 v120, v120
	v_mul_f32_e32 v93, 0xbfb8aa3b, v106
	v_exp_f32_e32 v93, v93
	v_add_f32_e32 v91, 1.0, v91
	v_rcp_f32_e32 v91, v91
	v_mul_f32_e32 v118, v118, v120
	v_pk_mul_f32 v[104:105], v[146:147], v[140:141] op_sel_hi:[0,1]
	v_cvt_pk_fp8_f32 v112, v99, v118 op_sel:[0,0,1]
	v_mul_f32_e32 v99, v108, v109
	v_add_f32_e32 v93, 1.0, v93
	v_mul_f32_e32 v91, v99, v91
	v_rcp_f32_e32 v93, v93
	v_mul_f32_e32 v99, 0xbfb8aa3b, v104
	v_exp_f32_e32 v99, v99
	v_pk_mul_f32 v[100:101], v[146:147], v[142:143] op_sel_hi:[0,1]
	v_mul_f32_e32 v106, v106, v107
	v_mul_f32_e32 v93, v106, v93
	v_mul_f32_e32 v104, v104, v105
	v_mul_f32_e32 v105, 0xbfb8aa3b, v100
	v_mul_f32_e32 v106, 0xbfb8aa3b, v102
	v_mul_f32_e32 v100, v100, v101
	v_mul_f32_e32 v101, v102, v103
	v_mul_f32_e32 v102, 0xbfb8aa3b, v96
	v_mul_f32_e32 v103, 0xbfb8aa3b, v88
	v_add_f32_e32 v99, 1.0, v99
	v_exp_f32_e32 v102, v102
	v_exp_f32_e32 v103, v103
	v_rcp_f32_e32 v99, v99
	v_exp_f32_e32 v105, v105
	v_exp_f32_e32 v106, v106
	v_mul_f32_e32 v96, v96, v97
	v_add_f32_e32 v97, 1.0, v102
	v_add_f32_e32 v102, 1.0, v103
	v_mul_f32_e32 v103, 0xbfb8aa3b, v86
	v_mul_f32_e32 v99, v104, v99
	v_add_f32_e32 v104, 1.0, v105
	v_add_f32_e32 v105, 1.0, v106
	v_rcp_f32_e32 v97, v97
	v_rcp_f32_e32 v102, v102
	v_exp_f32_e32 v103, v103
	v_rcp_f32_e32 v105, v105
	v_mul_f32_e32 v88, v88, v89
	v_mul_f32_e32 v96, v96, v97
	v_mul_f32_e32 v97, v88, v102
	v_add_f32_e32 v88, 1.0, v103
	v_rcp_f32_e32 v104, v104
	v_mul_f32_e32 v101, v101, v105
	v_rcp_f32_e32 v102, v88
	v_mov_b32_e32 v88, 0
	v_mov_b32_e32 v89, 0
	v_cvt_pk_fp8_f32 v88, v91, v93
	v_cvt_pk_fp8_f32 v89, v101, v96
	s_lshr_b32 s17, s15, 31
	s_lshr_b32 s15, s15, 3
	s_add_i32 s15, s15, s17
	v_mul_f32_e32 v86, v86, v87
	s_mul_i32 s15, s15, 44
	v_mul_f32_e32 v100, v100, v104
	v_mul_f32_e32 v86, v86, v102
	s_sub_i32 s15, s46, s15
	v_mov_b64_e32 v[12:13], s[8:9]
	v_or_b32_e32 v95, 16, v130
	v_cvt_pk_fp8_f32 v88, v99, v100 op_sel:[0,0,1]
	v_cvt_pk_fp8_f32 v89, v97, v86 op_sel:[0,0,1]
	v_mul_f32_e32 v86, 0xbfb8aa3b, v84
	v_lshl_or_b32 v6, s15, 7, v192
	v_mad_i64_i32 v[110:111], s[24:25], v95, s45, v[12:13]
	v_or_b32_e32 v95, 32, v130
	v_exp_f32_e32 v91, v86
	v_ashrrev_i32_e32 v7, 31, v6
	v_mad_i64_i32 v[86:87], s[24:25], v95, s45, v[12:13]
	v_lshl_add_u64 v[86:87], v[86:87], 0, v[6:7]
	global_store_dwordx2 v[86:87], v[88:89], off
	v_mul_f32_e32 v87, 0xbfb8aa3b, v82
	v_add_f32_e32 v86, 1.0, v91
	v_exp_f32_e32 v87, v87
	v_rcp_f32_e32 v86, v86
	v_mul_f32_e32 v84, v84, v85
	v_mul_f32_e32 v82, v82, v83
	v_add_f32_e32 v85, 1.0, v87
	v_mul_f32_e32 v84, v84, v86
	v_rcp_f32_e32 v85, v85
	v_mul_f32_e32 v86, 0xbfb8aa3b, v80
	v_exp_f32_e32 v86, v86
	v_mul_f32_e32 v83, 0xbfb8aa3b, v78
	v_mul_f32_e32 v82, v82, v85
	v_mul_f32_e32 v85, 0xbfb8aa3b, v76
	v_mul_f32_e32 v78, v78, v79
	v_mul_f32_e32 v76, v76, v77
	v_mul_f32_e32 v77, 0xbfb8aa3b, v74
	v_mul_f32_e32 v79, 0xbfb8aa3b, v72
	v_mul_f32_e32 v80, v80, v81
	v_add_f32_e32 v81, 1.0, v86
	v_exp_f32_e32 v77, v77
	v_exp_f32_e32 v79, v79
	v_rcp_f32_e32 v81, v81
	v_exp_f32_e32 v83, v83
	v_exp_f32_e32 v85, v85
	v_mul_f32_e32 v74, v74, v75
	v_add_f32_e32 v75, 1.0, v77
	v_add_f32_e32 v77, 1.0, v79
	v_mul_f32_e32 v79, 0xbfb8aa3b, v70
	v_mul_f32_e32 v80, v80, v81
	v_add_f32_e32 v81, 1.0, v83
	v_add_f32_e32 v83, 1.0, v85
	v_rcp_f32_e32 v75, v75
	v_rcp_f32_e32 v77, v77
	v_exp_f32_e32 v79, v79
	v_rcp_f32_e32 v83, v83
	v_mul_f32_e32 v72, v72, v73
	v_mul_f32_e32 v74, v74, v75
	v_mul_f32_e32 v75, v72, v77
	v_add_f32_e32 v72, 1.0, v79
	v_rcp_f32_e32 v81, v81
	v_mul_f32_e32 v76, v76, v83
	v_rcp_f32_e32 v77, v72
	v_mov_b32_e32 v72, 0
	v_mov_b32_e32 v73, 0
	v_cvt_pk_fp8_f32 v72, v84, v82
	v_cvt_pk_fp8_f32 v73, v76, v74
	v_mul_f32_e32 v70, v70, v71
	v_mul_f32_e32 v78, v78, v81
	v_mul_f32_e32 v70, v70, v77
	v_cvt_pk_fp8_f32 v72, v80, v78 op_sel:[0,0,1]
	v_cvt_pk_fp8_f32 v73, v75, v70 op_sel:[0,0,1]
	v_or_b32_e32 v88, 48, v130
	v_mad_i64_i32 v[70:71], s[24:25], v88, s45, v[12:13]
	v_lshl_add_u64 v[70:71], v[70:71], 0, v[6:7]
	global_store_dwordx2 v[70:71], v[72:73], off
	v_mul_f32_e32 v70, 0xbfb8aa3b, v68
	v_exp_f32_e32 v72, v70
	v_mul_f32_e32 v70, 0xbfb8aa3b, v66
	v_mul_f32_e32 v68, v68, v69
	v_mul_f32_e32 v66, v66, v67
	v_mul_f32_e32 v67, 0xbfb8aa3b, v64
	v_mul_f32_e32 v69, 0xbfb8aa3b, v62
	v_exp_f32_e32 v67, v67
	v_exp_f32_e32 v69, v69
	v_mul_f32_e32 v64, v64, v65
	v_mul_f32_e32 v62, v62, v63
	v_add_f32_e32 v65, 1.0, v67
	v_add_f32_e32 v67, 1.0, v69
	v_mul_f32_e32 v69, 0xbfb8aa3b, v60
	v_rcp_f32_e32 v65, v65
	v_exp_f32_e32 v69, v69
	v_mul_f32_e32 v60, v60, v61
	v_mul_f32_e32 v61, 0xbfb8aa3b, v56
	v_mul_f32_e32 v64, v64, v65
	v_add_f32_e32 v63, 1.0, v69
	v_mul_f32_e32 v65, 0xbfb8aa3b, v58
	v_rcp_f32_e32 v63, v63
	v_exp_f32_e32 v65, v65
	v_mul_f32_e32 v58, v58, v59
	v_exp_f32_e32 v73, v70
	v_mul_f32_e32 v60, v60, v63
	v_add_f32_e32 v59, 1.0, v65
	v_mul_f32_e32 v63, 0xbfb8aa3b, v54
	v_rcp_f32_e32 v59, v59
	v_exp_f32_e32 v61, v61
	v_exp_f32_e32 v63, v63
	v_add_f32_e32 v72, 1.0, v72
	v_add_f32_e32 v73, 1.0, v73
	v_mul_f32_e32 v58, v58, v59
	v_add_f32_e32 v59, 1.0, v61
	v_add_f32_e32 v61, 1.0, v63
	v_rcp_f32_e32 v72, v72
	v_rcp_f32_e32 v73, v73
	v_rcp_f32_e32 v61, v61
	v_rcp_f32_e32 v59, v59
	v_mul_f32_e32 v54, v54, v55
	v_mov_b32_e32 v55, 0
	v_cvt_pk_fp8_f32 v55, v60, v58
	v_mul_f32_e32 v68, v68, v72
	v_mul_f32_e32 v66, v66, v73
	v_rcp_f32_e32 v67, v67
	v_mul_f32_e32 v61, v54, v61
	v_mov_b32_e32 v54, 0
	v_mul_f32_e32 v56, v56, v57
	v_cvt_pk_fp8_f32 v54, v68, v66
	v_mul_f32_e32 v59, v56, v59
	v_cvt_pk_fp8_f32 v55, v59, v61 op_sel:[0,0,1]
	v_mul_f32_e32 v59, 0xbfb8aa3b, v50
	v_mul_f32_e32 v62, v62, v67
	v_exp_f32_e32 v59, v59
	v_cvt_pk_fp8_f32 v54, v64, v62 op_sel:[0,0,1]
	v_mad_i64_i32 v[70:71], s[24:25], v98, s45, v[12:13]
	v_mul_f32_e32 v56, 0xbfb8aa3b, v52
	v_exp_f32_e32 v58, v56
	v_lshl_add_u64 v[56:57], v[70:71], 0, v[6:7]
	v_mul_f32_e32 v52, v52, v53
	v_add_f32_e32 v53, 1.0, v59
	global_store_dwordx2 v[56:57], v[54:55], off
	v_rcp_f32_e32 v53, v53
	v_mul_f32_e32 v54, 0xbfb8aa3b, v48
	v_exp_f32_e32 v54, v54
	v_mul_f32_e32 v50, v50, v51
	v_mul_f32_e32 v50, v50, v53
	v_mul_f32_e32 v51, 0xbfb8aa3b, v46
	v_mul_f32_e32 v53, 0xbfb8aa3b, v44
	v_mul_f32_e32 v46, v46, v47
	v_mul_f32_e32 v44, v44, v45
	v_mul_f32_e32 v45, 0xbfb8aa3b, v42
	v_mul_f32_e32 v47, 0xbfb8aa3b, v40
	v_mul_f32_e32 v48, v48, v49
	v_add_f32_e32 v49, 1.0, v54
	v_exp_f32_e32 v45, v45
	v_exp_f32_e32 v47, v47
	v_rcp_f32_e32 v49, v49
	v_exp_f32_e32 v51, v51
	v_exp_f32_e32 v53, v53
	v_mul_f32_e32 v42, v42, v43
	v_add_f32_e32 v43, 1.0, v45
	v_add_f32_e32 v45, 1.0, v47
	v_mul_f32_e32 v47, 0xbfb8aa3b, v38
	v_add_f32_e32 v58, 1.0, v58
	v_mul_f32_e32 v48, v48, v49
	v_add_f32_e32 v49, 1.0, v51
	v_add_f32_e32 v51, 1.0, v53
	v_rcp_f32_e32 v43, v43
	v_rcp_f32_e32 v45, v45
	v_exp_f32_e32 v47, v47
	v_rcp_f32_e32 v58, v58
	v_rcp_f32_e32 v51, v51
	v_mul_f32_e32 v40, v40, v41
	v_mul_f32_e32 v42, v42, v43
	v_mul_f32_e32 v43, v40, v45
	v_add_f32_e32 v40, 1.0, v47
	v_mul_f32_e32 v52, v52, v58
	v_rcp_f32_e32 v49, v49
	v_mul_f32_e32 v44, v44, v51
	v_rcp_f32_e32 v45, v40
	v_mov_b32_e32 v40, 0
	v_mov_b32_e32 v41, 0
	v_cvt_pk_fp8_f32 v40, v52, v50
	v_cvt_pk_fp8_f32 v41, v44, v42
	v_mul_f32_e32 v38, v38, v39
	v_mul_f32_e32 v46, v46, v49
	v_mul_f32_e32 v38, v38, v45
	v_cvt_pk_fp8_f32 v40, v48, v46 op_sel:[0,0,1]
	v_cvt_pk_fp8_f32 v41, v43, v38 op_sel:[0,0,1]
	v_mad_i64_i32 v[38:39], s[24:25], v92, s45, v[12:13]
	v_lshl_add_u64 v[38:39], v[38:39], 0, v[6:7]
	global_store_dwordx2 v[38:39], v[40:41], off
	v_mul_f32_e32 v38, 0xbfb8aa3b, v36
	v_exp_f32_e32 v40, v38
	v_mul_f32_e32 v38, 0xbfb8aa3b, v34
	v_mul_f32_e32 v36, v36, v37
	v_mul_f32_e32 v34, v34, v35
	v_mul_f32_e32 v35, 0xbfb8aa3b, v32
	v_mul_f32_e32 v37, 0xbfb8aa3b, v30
	v_exp_f32_e32 v35, v35
	v_exp_f32_e32 v37, v37
	v_mul_f32_e32 v32, v32, v33
	v_mul_f32_e32 v30, v30, v31
	v_add_f32_e32 v33, 1.0, v35
	v_add_f32_e32 v35, 1.0, v37
	v_mul_f32_e32 v37, 0xbfb8aa3b, v28
	v_rcp_f32_e32 v33, v33
	v_exp_f32_e32 v37, v37
	v_mul_f32_e32 v28, v28, v29
	v_mul_f32_e32 v29, 0xbfb8aa3b, v24
	v_mul_f32_e32 v32, v32, v33
	v_add_f32_e32 v31, 1.0, v37
	v_mul_f32_e32 v33, 0xbfb8aa3b, v26
	v_rcp_f32_e32 v31, v31
	v_exp_f32_e32 v33, v33
	v_mul_f32_e32 v26, v26, v27
	v_exp_f32_e32 v41, v38
	v_mul_f32_e32 v28, v28, v31
	v_add_f32_e32 v27, 1.0, v33
	v_mul_f32_e32 v31, 0xbfb8aa3b, v22
	v_rcp_f32_e32 v27, v27
	v_exp_f32_e32 v29, v29
	v_exp_f32_e32 v31, v31
	v_add_f32_e32 v40, 1.0, v40
	v_add_f32_e32 v41, 1.0, v41
	v_mul_f32_e32 v26, v26, v27
	v_add_f32_e32 v27, 1.0, v29
	v_add_f32_e32 v29, 1.0, v31
	v_rcp_f32_e32 v40, v40
	v_rcp_f32_e32 v41, v41
	v_rcp_f32_e32 v29, v29
	v_rcp_f32_e32 v27, v27
	v_mul_f32_e32 v22, v22, v23
	v_mov_b32_e32 v23, 0
	v_mul_f32_e32 v36, v36, v40
	v_mul_f32_e32 v34, v34, v41
	v_rcp_f32_e32 v35, v35
	v_mul_f32_e32 v29, v22, v29
	v_mov_b32_e32 v22, 0
	v_cvt_pk_fp8_f32 v23, v28, v26
	v_cvt_pk_fp8_f32 v22, v36, v34
	v_mul_f32_e32 v24, v24, v25
	v_mul_f32_e32 v27, v24, v27
	v_mul_f32_e32 v30, v30, v35
	v_cvt_pk_fp8_f32 v23, v27, v29 op_sel:[0,0,1]
	v_mul_f32_e32 v27, 0xbfb8aa3b, v16
	v_cvt_pk_fp8_f32 v22, v32, v30 op_sel:[0,0,1]
	v_exp_f32_e32 v27, v27
	v_mad_i64_i32 v[38:39], s[24:25], v94, s45, v[12:13]
	v_mul_f32_e32 v24, 0xbfb8aa3b, v20
	v_exp_f32_e32 v26, v24
	v_lshl_add_u64 v[24:25], v[38:39], 0, v[6:7]
	global_store_dwordx2 v[24:25], v[22:23], off
	v_mul_f32_e32 v20, v20, v21
	v_add_f32_e32 v21, 1.0, v27
	v_mul_f32_e32 v22, 0xbfb8aa3b, v14
	v_rcp_f32_e32 v21, v21
	v_exp_f32_e32 v22, v22
	v_mul_f32_e32 v16, v16, v17
	v_mul_f32_e32 v14, v14, v15
	v_mul_f32_e32 v16, v16, v21
	v_add_f32_e32 v15, 1.0, v22
	v_mul_f32_e32 v17, 0xbfb8aa3b, v8
	v_mul_f32_e32 v21, 0xbfb8aa3b, v18
	v_rcp_f32_e32 v15, v15
	v_exp_f32_e32 v17, v17
	v_exp_f32_e32 v21, v21
	v_mul_f32_e32 v8, v8, v9
	v_mul_f32_e32 v14, v14, v15
	v_add_f32_e32 v15, 1.0, v17
	v_add_f32_e32 v17, 1.0, v21
	v_rcp_f32_e32 v15, v15
	v_rcp_f32_e32 v17, v17
	v_mul_f32_e32 v9, v18, v19
	v_add_f32_e32 v26, 1.0, v26
	v_mul_f32_e32 v8, v8, v15
	v_mul_f32_e32 v9, v9, v17
	v_mul_f32_e32 v15, 0xbfb8aa3b, v10
	v_mul_f32_e32 v17, 0xbfb8aa3b, v4
	v_exp_f32_e32 v15, v15
	v_exp_f32_e32 v17, v17
	v_mul_f32_e32 v10, v10, v11
	v_rcp_f32_e32 v26, v26
	v_add_f32_e32 v11, 1.0, v15
	v_add_f32_e32 v15, 1.0, v17
	v_mul_f32_e32 v17, 0xbfb8aa3b, v2
	v_rcp_f32_e32 v11, v11
	v_rcp_f32_e32 v15, v15
	v_exp_f32_e32 v17, v17
	v_mul_f32_e32 v4, v4, v5
	v_mul_f32_e32 v10, v10, v11
	v_mul_f32_e32 v11, v4, v15
	v_add_f32_e32 v4, 1.0, v17
	v_mul_f32_e32 v20, v20, v26
	v_rcp_f32_e32 v15, v4
	v_mov_b32_e32 v4, 0
	v_mov_b32_e32 v5, 0
	v_cvt_pk_fp8_f32 v4, v20, v16
	v_cvt_pk_fp8_f32 v5, v9, v10
	v_mul_f32_e32 v2, v2, v3
	v_mul_f32_e32 v2, v2, v15
	v_cvt_pk_fp8_f32 v4, v14, v8 op_sel:[0,0,1]
	v_cvt_pk_fp8_f32 v5, v11, v2 op_sel:[0,0,1]
	v_mad_i64_i32 v[126:127], s[24:25], v130, s45, v[12:13]
	v_mad_i64_i32 v[2:3], s[24:25], v90, s45, v[12:13]
	v_readlane_b32 s48, v250, 56
	v_lshl_add_u64 v[126:127], v[126:127], 0, v[6:7]
	v_lshl_add_u64 v[110:111], v[110:111], 0, v[6:7]
	v_lshl_add_u64 v[2:3], v[2:3], 0, v[6:7]
	s_andn2_b64 vcc, exec, s[0:1]
	s_mov_b64 s[0:1], -1
	v_readlane_b32 s60, v251, 4
	v_readlane_b32 s61, v251, 5
	v_readlane_b32 s62, v251, 6
	v_readlane_b32 s63, v251, 7
	global_store_dwordx2 v[126:127], v[128:129], off
	global_store_dwordx2 v[110:111], v[112:113], off
	global_store_dwordx2 v[2:3], v[4:5], off
	v_readlane_b32 s49, v250, 57
	v_readlane_b32 s50, v250, 58
	v_readlane_b32 s51, v250, 59
	v_readlane_b32 s52, v250, 60
	v_readlane_b32 s53, v250, 61
	v_readlane_b32 s54, v250, 62
	v_readlane_b32 s55, v250, 63
	v_readlane_b32 s56, v251, 0
	v_readlane_b32 s57, v251, 1
	v_readlane_b32 s58, v251, 2
	v_readlane_b32 s59, v251, 3
	s_cbranch_vccnz .LBB0_760
	s_andn2_b64 vcc, exec, s[4:5]
	s_cbranch_vccnz .LBB0_759
	s_barrier
	s_branch .LBB0_759

.LBB0_1722:
	s_ashr_i32 s37, s36, 31
	s_lshl_b64 s[40:41], s[36:37], 19
	s_add_u32 s40, s63, s40
	s_addc_u32 s41, s64, s41
	s_and_b64 s[44:45], s[42:43], exec
	s_cselect_b32 s37, s41, s51
	s_cselect_b32 s84, s40, s50
	s_ashr_i32 s39, s38, 31
	s_lshl_b64 s[44:45], s[38:39], 19
	s_add_u32 s44, s65, s44
	s_addc_u32 s45, s66, s45
	s_and_b64 s[54:55], s[42:43], exec
	s_cselect_b32 s39, s45, s53
	s_cselect_b32 s85, s44, s52
	s_add_u32 s50, s50, 0x40080
	s_addc_u32 s51, s51, 0
	s_add_u32 s86, s52, 0x100
	v_mov_b32_e32 v2, 0
	s_addc_u32 s87, s53, 0
	s_mov_b32 s88, -2
	v_mov_b32_e32 v3, v2
	v_mov_b32_e32 v4, v2
	v_mov_b32_e32 v5, v2
	v_mov_b32_e32 v6, v2
	v_mov_b32_e32 v7, v2
	v_mov_b32_e32 v8, v2
	v_mov_b32_e32 v9, v2
	v_mov_b32_e32 v14, v2
	v_mov_b32_e32 v15, v2
	v_mov_b32_e32 v16, v2
	v_mov_b32_e32 v17, v2
	v_mov_b32_e32 v22, v2
	v_mov_b32_e32 v23, v2
	v_mov_b32_e32 v24, v2
	v_mov_b32_e32 v25, v2
	v_mov_b32_e32 v30, v2
	v_mov_b32_e32 v31, v2
	v_mov_b32_e32 v32, v2
	v_mov_b32_e32 v33, v2
	v_mov_b32_e32 v38, v2
	v_mov_b32_e32 v39, v2
	v_mov_b32_e32 v40, v2
	v_mov_b32_e32 v41, v2
	v_mov_b32_e32 v46, v2
	v_mov_b32_e32 v47, v2
	v_mov_b32_e32 v48, v2
	v_mov_b32_e32 v49, v2
	v_mov_b32_e32 v54, v2
	v_mov_b32_e32 v55, v2
	v_mov_b32_e32 v56, v2
	v_mov_b32_e32 v57, v2
	v_mov_b32_e32 v10, v2
	v_mov_b32_e32 v11, v2
	v_mov_b32_e32 v12, v2
	v_mov_b32_e32 v13, v2
	v_mov_b32_e32 v18, v2
	v_mov_b32_e32 v19, v2
	v_mov_b32_e32 v20, v2
	v_mov_b32_e32 v21, v2
	v_mov_b32_e32 v26, v2
	v_mov_b32_e32 v27, v2
	v_mov_b32_e32 v28, v2
	v_mov_b32_e32 v29, v2
	v_mov_b32_e32 v34, v2
	v_mov_b32_e32 v35, v2
	v_mov_b32_e32 v36, v2
	v_mov_b32_e32 v37, v2
	v_mov_b32_e32 v42, v2
	v_mov_b32_e32 v43, v2
	v_mov_b32_e32 v44, v2
	v_mov_b32_e32 v45, v2
	v_mov_b32_e32 v50, v2
	v_mov_b32_e32 v51, v2
	v_mov_b32_e32 v52, v2
	v_mov_b32_e32 v53, v2
	v_mov_b32_e32 v58, v2
	v_mov_b32_e32 v59, v2
	v_mov_b32_e32 v60, v2
	v_mov_b32_e32 v61, v2
	v_mov_b32_e32 v62, v2
	v_mov_b32_e32 v63, v2
	v_mov_b32_e32 v64, v2
	v_mov_b32_e32 v65, v2
	v_mov_b32_e32 v66, v2
	v_mov_b32_e32 v67, v2
	v_mov_b32_e32 v68, v2
	v_mov_b32_e32 v69, v2
	v_mov_b32_e32 v70, v2
	v_mov_b32_e32 v71, v2
	v_mov_b32_e32 v72, v2
	v_mov_b32_e32 v73, v2
	v_mov_b32_e32 v78, v2
	v_mov_b32_e32 v79, v2
	v_mov_b32_e32 v80, v2
	v_mov_b32_e32 v81, v2
	v_mov_b32_e32 v90, v2
	v_mov_b32_e32 v91, v2
	v_mov_b32_e32 v92, v2
	v_mov_b32_e32 v93, v2
	v_mov_b32_e32 v98, v2
	v_mov_b32_e32 v99, v2
	v_mov_b32_e32 v100, v2
	v_mov_b32_e32 v101, v2
	v_mov_b32_e32 v102, v2
	v_mov_b32_e32 v103, v2
	v_mov_b32_e32 v104, v2
	v_mov_b32_e32 v105, v2
	v_mov_b32_e32 v106, v2
	v_mov_b32_e32 v107, v2
	v_mov_b32_e32 v108, v2
	v_mov_b32_e32 v109, v2
	v_mov_b32_e32 v122, v2
	v_mov_b32_e32 v123, v2
	v_mov_b32_e32 v124, v2
	v_mov_b32_e32 v125, v2
	v_mov_b32_e32 v74, v2
	v_mov_b32_e32 v75, v2
	v_mov_b32_e32 v76, v2
	v_mov_b32_e32 v77, v2
	v_mov_b32_e32 v82, v2
	v_mov_b32_e32 v83, v2
	v_mov_b32_e32 v84, v2
	v_mov_b32_e32 v85, v2
	v_mov_b32_e32 v86, v2
	v_mov_b32_e32 v87, v2
	v_mov_b32_e32 v88, v2
	v_mov_b32_e32 v89, v2
	v_mov_b32_e32 v94, v2
	v_mov_b32_e32 v95, v2
	v_mov_b32_e32 v96, v2
	v_mov_b32_e32 v97, v2
	v_mov_b32_e32 v110, v2
	v_mov_b32_e32 v111, v2
	v_mov_b32_e32 v112, v2
	v_mov_b32_e32 v113, v2
	v_mov_b32_e32 v114, v2
	v_mov_b32_e32 v115, v2
	v_mov_b32_e32 v116, v2
	v_mov_b32_e32 v117, v2
	v_mov_b32_e32 v118, v2
	v_mov_b32_e32 v119, v2
	v_mov_b32_e32 v120, v2
	v_mov_b32_e32 v121, v2
	v_mov_b32_e32 v126, v2
	v_mov_b32_e32 v127, v2
	v_mov_b32_e32 v128, v2
	v_mov_b32_e32 v129, v2
	v_lshl_add_u32 v234, s48, 8, v179
	v_ashrrev_i32_e32 v235, 31, v234
	v_lshl_add_u64 v[236:237], v[234:235], 2, s[24:25]
	global_load_dword v240, v[236:237], off
	global_load_dword v241, v[236:237], off offset:64
	global_load_dword v242, v[236:237], off offset:128
	global_load_dword v243, v[236:237], off offset:192
	global_load_dword v244, v[236:237], off offset:512
	global_load_dword v245, v[236:237], off offset:576
	global_load_dword v246, v[236:237], off offset:640
	global_load_dword v247, v[236:237], off offset:704

.LBB0_1726:
	v_lshl_add_u32 v130, s48, 8, v179
	v_ashrrev_i32_e32 v131, 31, v130
	s_nop 15
	s_nop 15
	v_lshl_add_u64 v[134:135], v[130:131], 2, s[24:25]
	v_mov_b32_e32 v131, v240
	v_mov_b32_e32 v144, v241
	v_mov_b32_e32 v145, v242
	v_mov_b32_e32 v150, v243
	v_cvt_f32_i32_e32 v138, v110
	v_add_u32_e32 v110, 0x80, v130
	v_cvt_f32_i32_e32 v139, v98
	v_cvt_f32_i32_e32 v98, v111
	v_ashrrev_i32_e32 v111, 31, v110
	v_lshl_add_u64 v[110:111], v[110:111], 2, s[24:25]
	v_mov_b32_e32 v151, v244
	v_cvt_f32_i32_e32 v142, v94
	v_cvt_f32_i32_e32 v94, v96
	v_add_u32_e32 v96, 0x90, v130
	v_cvt_f32_i32_e32 v140, v112
	v_cvt_f32_i32_e32 v143, v90
	v_cvt_f32_i32_e32 v90, v95
	v_cvt_f32_i32_e32 v95, v92
	v_cvt_f32_i32_e32 v92, v97
	v_add_u32_e32 v110, 0xa0, v130
	v_add_u32_e32 v112, 0xb0, v130
	v_ashrrev_i32_e32 v97, 31, v96
	v_cvt_f32_i32_e32 v141, v100
	v_cvt_f32_i32_e32 v100, v113
	v_ashrrev_i32_e32 v111, 31, v110
	v_ashrrev_i32_e32 v113, 31, v112
	v_lshl_add_u64 v[96:97], v[96:97], 2, s[24:25]
	v_lshl_add_u64 v[110:111], v[110:111], 2, s[24:25]
	v_lshl_add_u64 v[112:113], v[112:113], 2, s[24:25]
	v_mov_b32_e32 v152, v245
	v_mov_b32_e32 v153, v246
	v_mov_b32_e32 v154, v247
	v_cvt_f32_i32_e32 v133, v122
	v_cvt_f32_i32_e32 v122, v127
	v_cvt_f32_i32_e32 v127, v124
	v_cvt_f32_i32_e32 v124, v129
	v_cvt_f32_i32_e32 v129, v106
	v_cvt_f32_i32_e32 v107, v107
	v_cvt_f32_i32_e32 v106, v119
	v_cvt_f32_i32_e32 v99, v99
	v_cvt_f32_i32_e32 v91, v91
	v_cvt_f32_i32_e32 v132, v126
	v_cvt_f32_i32_e32 v123, v123
	v_cvt_f32_i32_e32 v126, v128
	v_cvt_f32_i32_e32 v125, v125
	v_cvt_f32_i32_e32 v128, v118
	v_cvt_f32_i32_e32 v119, v108
	v_cvt_f32_i32_e32 v118, v120
	v_cvt_f32_i32_e32 v109, v109
	v_cvt_f32_i32_e32 v108, v121
	v_cvt_f32_i32_e32 v79, v79
	v_cvt_f32_i32_e32 v81, v81
	v_cvt_f32_i32_e32 v71, v71
	v_cvt_f32_i32_e32 v73, v73
	v_cvt_f32_i32_e32 v67, v67
	v_cvt_f32_i32_e32 v69, v69
	v_cvt_f32_i32_e32 v55, v55
	v_cvt_f32_i32_e32 v57, v57
	v_cvt_f32_i32_e32 v47, v47
	v_cvt_f32_i32_e32 v49, v49
	v_cvt_f32_i32_e32 v39, v39
	v_cvt_f32_i32_e32 v41, v41
	v_cvt_f32_i32_e32 v31, v31
	v_cvt_f32_i32_e32 v33, v33
	v_cvt_f32_i32_e32 v23, v23
	v_cvt_f32_i32_e32 v25, v25
	v_cvt_f32_i32_e32 v15, v15
	v_cvt_f32_i32_e32 v17, v17
	v_cvt_f32_i32_e32 v7, v7
	v_cvt_f32_i32_e32 v9, v9
	v_cvt_f32_i32_e32 v135, v102
	v_cvt_f32_i32_e32 v134, v114
	v_cvt_f32_i32_e32 v103, v103
	v_cvt_f32_i32_e32 v102, v115
	v_cvt_f32_i32_e32 v137, v104
	v_cvt_f32_i32_e32 v136, v116
	v_cvt_f32_i32_e32 v105, v105
	v_cvt_f32_i32_e32 v104, v117
	v_cvt_f32_i32_e32 v101, v101
	v_cvt_f32_i32_e32 v3, v3
	s_mul_hi_i32 s37, s46, 0x92492493
	s_add_i32 s37, s37, s46
	s_waitcnt vmcnt(8)
	v_mul_f32_e32 v96, v1, v131
	v_mul_f32_e32 v130, v1, v144
	v_mul_f32_e32 v144, v1, v145
	v_pk_mul_f32 v[148:149], v[96:97], v[106:107] op_sel_hi:[0,1]
	v_pk_mul_f32 v[106:107], v[130:131], v[98:99] op_sel_hi:[0,1]
	v_pk_mul_f32 v[98:99], v[144:145], v[90:91] op_sel_hi:[0,1]
	v_cvt_f32_i32_e32 v91, v78
	v_cvt_f32_i32_e32 v90, v86
	v_cvt_f32_i32_e32 v78, v87
	v_cvt_f32_i32_e32 v87, v80
	v_cvt_f32_i32_e32 v86, v88
	v_cvt_f32_i32_e32 v80, v89
	v_pk_mul_f32 v[132:133], v[96:97], v[132:133] op_sel_hi:[0,1]
	v_pk_mul_f32 v[146:147], v[96:97], v[122:123] op_sel_hi:[0,1]
	v_pk_mul_f32 v[126:127], v[96:97], v[126:127] op_sel_hi:[0,1]
	v_pk_mul_f32 v[124:125], v[96:97], v[124:125] op_sel_hi:[0,1]
	v_pk_mul_f32 v[128:129], v[96:97], v[128:129] op_sel_hi:[0,1]
	v_pk_mul_f32 v[120:121], v[96:97], v[118:119] op_sel_hi:[0,1]
	v_pk_mul_f32 v[118:119], v[96:97], v[108:109] op_sel_hi:[0,1]
	v_pk_mul_f32 v[96:97], v[144:145], v[94:95] op_sel_hi:[0,1]
	v_pk_mul_f32 v[94:95], v[144:145], v[90:91] op_sel_hi:[0,1]
	v_pk_mul_f32 v[90:91], v[144:145], v[78:79] op_sel_hi:[0,1]
	v_cvt_f32_i32_e32 v79, v70
	v_cvt_f32_i32_e32 v70, v83
	v_pk_mul_f32 v[88:89], v[144:145], v[86:87] op_sel_hi:[0,1]
	v_pk_mul_f32 v[86:87], v[144:145], v[80:81] op_sel_hi:[0,1]
	v_mul_f32_e32 v122, v1, v150
	v_cvt_f32_i32_e32 v78, v82
	v_cvt_f32_i32_e32 v81, v72
	v_cvt_f32_i32_e32 v72, v85
	v_pk_mul_f32 v[82:83], v[122:123], v[70:71] op_sel_hi:[0,1]
	v_cvt_f32_i32_e32 v71, v66
	v_cvt_f32_i32_e32 v66, v75
	v_cvt_f32_i32_e32 v80, v84
	v_pk_mul_f32 v[84:85], v[122:123], v[78:79] op_sel_hi:[0,1]
	v_pk_mul_f32 v[78:79], v[122:123], v[72:73] op_sel_hi:[0,1]
	v_cvt_f32_i32_e32 v70, v74
	v_cvt_f32_i32_e32 v73, v68
	v_cvt_f32_i32_e32 v72, v76
	v_cvt_f32_i32_e32 v68, v77
	v_pk_mul_f32 v[74:75], v[122:123], v[66:67] op_sel_hi:[0,1]
	v_cvt_f32_i32_e32 v67, v54
	v_cvt_f32_i32_e32 v66, v62
	v_cvt_f32_i32_e32 v54, v63
	v_pk_mul_f32 v[80:81], v[122:123], v[80:81] op_sel_hi:[0,1]
	v_pk_mul_f32 v[76:77], v[122:123], v[70:71] op_sel_hi:[0,1]
	v_pk_mul_f32 v[72:73], v[122:123], v[72:73] op_sel_hi:[0,1]
	v_pk_mul_f32 v[70:71], v[122:123], v[68:69] op_sel_hi:[0,1]
	v_mul_f32_e32 v122, v1, v151
	v_cvt_f32_i32_e32 v63, v56
	v_cvt_f32_i32_e32 v62, v64
	v_cvt_f32_i32_e32 v56, v65
	v_pk_mul_f32 v[68:69], v[122:123], v[66:67] op_sel_hi:[0,1]
	v_pk_mul_f32 v[66:67], v[122:123], v[54:55] op_sel_hi:[0,1]
	v_cvt_f32_i32_e32 v55, v46
	v_cvt_f32_i32_e32 v46, v59
	v_pk_mul_f32 v[64:65], v[122:123], v[62:63] op_sel_hi:[0,1]
	v_pk_mul_f32 v[62:63], v[122:123], v[56:57] op_sel_hi:[0,1]
	v_cvt_f32_i32_e32 v54, v58
	v_cvt_f32_i32_e32 v57, v48
	v_cvt_f32_i32_e32 v56, v60
	v_cvt_f32_i32_e32 v48, v61
	v_pk_mul_f32 v[58:59], v[122:123], v[46:47] op_sel_hi:[0,1]
	v_cvt_f32_i32_e32 v47, v38
	v_cvt_f32_i32_e32 v38, v51
	v_pk_mul_f32 v[60:61], v[122:123], v[54:55] op_sel_hi:[0,1]
	v_pk_mul_f32 v[56:57], v[122:123], v[56:57] op_sel_hi:[0,1]
	v_pk_mul_f32 v[54:55], v[122:123], v[48:49] op_sel_hi:[0,1]
	v_mul_f32_e32 v122, v1, v152
	v_cvt_f32_i32_e32 v46, v50
	v_cvt_f32_i32_e32 v49, v40
	v_cvt_f32_i32_e32 v40, v53
	v_pk_mul_f32 v[50:51], v[122:123], v[38:39] op_sel_hi:[0,1]
	v_cvt_f32_i32_e32 v39, v30
	v_cvt_f32_i32_e32 v30, v43
	v_cvt_f32_i32_e32 v48, v52
	v_pk_mul_f32 v[52:53], v[122:123], v[46:47] op_sel_hi:[0,1]
	v_pk_mul_f32 v[46:47], v[122:123], v[40:41] op_sel_hi:[0,1]
	v_cvt_f32_i32_e32 v38, v42
	v_cvt_f32_i32_e32 v41, v32
	v_cvt_f32_i32_e32 v40, v44
	v_cvt_f32_i32_e32 v32, v45
	v_pk_mul_f32 v[42:43], v[122:123], v[30:31] op_sel_hi:[0,1]
	v_cvt_f32_i32_e32 v31, v22
	v_cvt_f32_i32_e32 v22, v35
	v_pk_mul_f32 v[48:49], v[122:123], v[48:49] op_sel_hi:[0,1]
	v_pk_mul_f32 v[44:45], v[122:123], v[38:39] op_sel_hi:[0,1]
	v_pk_mul_f32 v[40:41], v[122:123], v[40:41] op_sel_hi:[0,1]
	v_pk_mul_f32 v[38:39], v[122:123], v[32:33] op_sel_hi:[0,1]
	v_mul_f32_e32 v122, v1, v153
	v_cvt_f32_i32_e32 v30, v34
	v_cvt_f32_i32_e32 v33, v24
	v_cvt_f32_i32_e32 v24, v37
	v_pk_mul_f32 v[34:35], v[122:123], v[22:23] op_sel_hi:[0,1]
	v_cvt_f32_i32_e32 v23, v14
	v_cvt_f32_i32_e32 v14, v27
	v_cvt_f32_i32_e32 v32, v36
	v_pk_mul_f32 v[36:37], v[122:123], v[30:31] op_sel_hi:[0,1]
	v_pk_mul_f32 v[30:31], v[122:123], v[24:25] op_sel_hi:[0,1]
	v_cvt_f32_i32_e32 v22, v26
	v_cvt_f32_i32_e32 v25, v16
	v_cvt_f32_i32_e32 v24, v28
	v_cvt_f32_i32_e32 v16, v29
	v_pk_mul_f32 v[26:27], v[122:123], v[14:15] op_sel_hi:[0,1]
	v_cvt_f32_i32_e32 v15, v6
	v_cvt_f32_i32_e32 v6, v19
	v_cvt_f32_i32_e32 v19, v8
	v_cvt_f32_i32_e32 v8, v21
	v_pk_mul_f32 v[32:33], v[122:123], v[32:33] op_sel_hi:[0,1]
	v_pk_mul_f32 v[28:29], v[122:123], v[22:23] op_sel_hi:[0,1]
	v_pk_mul_f32 v[24:25], v[122:123], v[24:25] op_sel_hi:[0,1]
	v_pk_mul_f32 v[22:23], v[122:123], v[16:17] op_sel_hi:[0,1]
	v_mul_f32_e32 v122, v1, v154
	v_cvt_f32_i32_e32 v14, v18
	v_cvt_f32_i32_e32 v18, v20
	v_pk_mul_f32 v[16:17], v[122:123], v[6:7] op_sel_hi:[0,1]
	v_pk_mul_f32 v[6:7], v[122:123], v[8:9] op_sel_hi:[0,1]
	v_cvt_f32_i32_e32 v9, v2
	v_cvt_f32_i32_e32 v8, v10
	v_pk_mul_f32 v[20:21], v[122:123], v[14:15] op_sel_hi:[0,1]
	v_pk_mul_f32 v[14:15], v[122:123], v[18:19] op_sel_hi:[0,1]
	v_pk_mul_f32 v[116:117], v[130:131], v[134:135] op_sel_hi:[0,1]
	v_pk_mul_f32 v[18:19], v[122:123], v[8:9] op_sel_hi:[0,1]
	v_mul_f32_e32 v8, 0xbfb8aa3b, v132
	v_pk_mul_f32 v[114:115], v[130:131], v[102:103] op_sel_hi:[0,1]
	v_pk_mul_f32 v[112:113], v[130:131], v[136:137] op_sel_hi:[0,1]
	v_pk_mul_f32 v[110:111], v[130:131], v[104:105] op_sel_hi:[0,1]
	v_pk_mul_f32 v[108:109], v[130:131], v[138:139] op_sel_hi:[0,1]
	v_pk_mul_f32 v[104:105], v[130:131], v[140:141] op_sel_hi:[0,1]
	v_pk_mul_f32 v[102:103], v[130:131], v[100:101] op_sel_hi:[0,1]
	v_cvt_f32_i32_e32 v130, v12
	v_exp_f32_e32 v12, v8
	v_cvt_f32_i32_e32 v2, v11
	v_cvt_f32_i32_e32 v131, v4
	v_cvt_f32_i32_e32 v135, v5
	v_cvt_f32_i32_e32 v134, v13
	v_add_f32_e32 v12, 1.0, v12
	v_pk_mul_f32 v[10:11], v[122:123], v[2:3] op_sel_hi:[0,1]
	v_pk_mul_f32 v[4:5], v[122:123], v[130:131] op_sel_hi:[0,1]
	v_pk_mul_f32 v[2:3], v[122:123], v[134:135] op_sel_hi:[0,1]
	v_rcp_f32_e32 v123, v12
	v_mul_f32_e32 v12, 0xbfb8aa3b, v146
	v_mul_f32_e32 v131, v132, v133
	v_exp_f32_e32 v130, v12
	v_mul_f32_e32 v123, v131, v123
	v_mul_f32_e32 v131, 0xbfb8aa3b, v126
	v_exp_f32_e32 v131, v131
	v_add_f32_e32 v130, 1.0, v130
	v_rcp_f32_e32 v130, v130
	v_mul_f32_e32 v126, v126, v127
	v_add_f32_e32 v127, 1.0, v131
	v_mul_f32_e32 v131, 0xbfb8aa3b, v124
	v_rcp_f32_e32 v127, v127
	v_exp_f32_e32 v131, v131
	v_mul_f32_e32 v132, v146, v147
	v_mul_f32_e32 v130, v132, v130
	v_mul_f32_e32 v132, 0xbfb8aa3b, v128
	v_exp_f32_e32 v132, v132
	v_mul_f32_e32 v126, v126, v127
	v_add_f32_e32 v127, 1.0, v131
	v_rcp_f32_e32 v127, v127
	v_add_f32_e32 v131, 1.0, v132
	v_mul_f32_e32 v124, v124, v125
	v_mul_f32_e32 v125, v128, v129
	v_mul_f32_e32 v128, 0xbfb8aa3b, v120
	v_rcp_f32_e32 v131, v131
	v_mul_f32_e32 v124, v124, v127
	v_mul_f32_e32 v127, 0xbfb8aa3b, v148
	v_exp_f32_e32 v128, v128
	v_exp_f32_e32 v127, v127
	v_mul_f32_e32 v125, v125, v131
	v_mul_f32_e32 v131, 0xbfb8aa3b, v118
	v_add_f32_e32 v128, 1.0, v128
	v_add_f32_e32 v127, 1.0, v127
	v_rcp_f32_e32 v128, v128
	v_exp_f32_e32 v131, v131
	v_rcp_f32_e32 v127, v127
	v_mul_f32_e32 v120, v120, v121
	v_mul_f32_e32 v129, v148, v149
	v_mul_f32_e32 v128, v120, v128
	v_add_f32_e32 v120, 1.0, v131
	v_mul_f32_e32 v127, v129, v127
	v_rcp_f32_e32 v129, v120
	v_mov_b32_e32 v120, 0
	v_mov_b32_e32 v121, 0
	v_cvt_pk_fp8_f32 v120, v123, v130
	v_cvt_pk_fp8_f32 v121, v125, v127
	s_lshr_b32 s39, s37, 31
	s_lshr_b32 s37, s37, 5
	s_add_i32 s37, s37, s39
	v_mul_f32_e32 v118, v118, v119
	s_mul_i32 s37, s37, 56
	v_mul_f32_e32 v118, v118, v129
	s_sub_i32 s37, s46, s37
	v_cvt_pk_fp8_f32 v120, v126, v124 op_sel:[0,0,1]
	v_cvt_pk_fp8_f32 v121, v128, v118 op_sel:[0,0,1]
	v_mul_f32_e32 v118, 0xbfb8aa3b, v116
	v_lshl_add_u32 v122, s83, 8, v179
	v_lshl_or_b32 v8, s37, 7, v186
	v_mov_b64_e32 v[12:13], s[26:27]
	v_exp_f32_e32 v123, v118
	v_ashrrev_i32_e32 v9, 31, v8
	v_mad_i64_i32 v[118:119], s[50:51], v122, s81, v[12:13]
	v_lshl_add_u64 v[118:119], v[118:119], 0, v[8:9]
	global_store_dwordx2 v[118:119], v[120:121], off
	v_mul_f32_e32 v119, 0xbfb8aa3b, v114
	v_add_f32_e32 v118, 1.0, v123
	v_exp_f32_e32 v119, v119
	v_rcp_f32_e32 v118, v118
	v_mul_f32_e32 v116, v116, v117
	v_mul_f32_e32 v114, v114, v115
	v_add_f32_e32 v117, 1.0, v119
	v_mul_f32_e32 v116, v116, v118
	v_rcp_f32_e32 v117, v117
	v_mul_f32_e32 v118, 0xbfb8aa3b, v112
	v_exp_f32_e32 v118, v118
	v_mul_f32_e32 v115, 0xbfb8aa3b, v110
	v_mul_f32_e32 v114, v114, v117
	v_mul_f32_e32 v117, 0xbfb8aa3b, v108
	v_mul_f32_e32 v110, v110, v111
	v_mul_f32_e32 v108, v108, v109
	v_mul_f32_e32 v109, 0xbfb8aa3b, v106
	v_mul_f32_e32 v111, 0xbfb8aa3b, v104
	v_mul_f32_e32 v112, v112, v113
	v_add_f32_e32 v113, 1.0, v118
	v_exp_f32_e32 v109, v109
	v_exp_f32_e32 v111, v111
	v_rcp_f32_e32 v113, v113
	v_exp_f32_e32 v115, v115
	v_exp_f32_e32 v117, v117
	v_mul_f32_e32 v106, v106, v107
	v_add_f32_e32 v107, 1.0, v109
	v_add_f32_e32 v109, 1.0, v111
	v_mul_f32_e32 v111, 0xbfb8aa3b, v102
	v_mul_f32_e32 v112, v112, v113
	v_add_f32_e32 v113, 1.0, v115
	v_add_f32_e32 v115, 1.0, v117
	v_rcp_f32_e32 v107, v107
	v_rcp_f32_e32 v109, v109
	v_exp_f32_e32 v111, v111
	v_rcp_f32_e32 v115, v115
	v_mul_f32_e32 v104, v104, v105
	v_mul_f32_e32 v106, v106, v107
	v_mul_f32_e32 v107, v104, v109
	v_add_f32_e32 v104, 1.0, v111
	v_rcp_f32_e32 v113, v113
	v_mul_f32_e32 v108, v108, v115
	v_rcp_f32_e32 v109, v104
	v_mov_b32_e32 v104, 0
	v_mov_b32_e32 v105, 0
	v_cvt_pk_fp8_f32 v104, v116, v114
	v_cvt_pk_fp8_f32 v105, v108, v106
	v_mul_f32_e32 v102, v102, v103
	v_pk_mul_f32 v[100:101], v[144:145], v[142:143] op_sel_hi:[0,1]
	v_mul_f32_e32 v110, v110, v113
	v_mul_f32_e32 v102, v102, v109
	v_cvt_pk_fp8_f32 v104, v112, v110 op_sel:[0,0,1]
	v_cvt_pk_fp8_f32 v105, v107, v102 op_sel:[0,0,1]
	v_mul_f32_e32 v102, 0xbfb8aa3b, v100
	v_or_b32_e32 v120, 16, v122
	v_exp_f32_e32 v106, v102
	v_mad_i64_i32 v[102:103], s[50:51], v120, s81, v[12:13]
	v_lshl_add_u64 v[102:103], v[102:103], 0, v[8:9]
	global_store_dwordx2 v[102:103], v[104:105], off
	v_mul_f32_e32 v103, 0xbfb8aa3b, v98
	v_add_f32_e32 v102, 1.0, v106
	v_exp_f32_e32 v103, v103
	v_rcp_f32_e32 v102, v102
	v_cvt_f32_i32_e32 v93, v93
	v_mul_f32_e32 v100, v100, v101
	v_add_f32_e32 v101, 1.0, v103
	v_mul_f32_e32 v100, v100, v102
	v_rcp_f32_e32 v101, v101
	v_mul_f32_e32 v102, 0xbfb8aa3b, v96
	v_exp_f32_e32 v102, v102
	v_pk_mul_f32 v[92:93], v[144:145], v[92:93] op_sel_hi:[0,1]
	v_mul_f32_e32 v98, v98, v99
	v_mul_f32_e32 v98, v98, v101
	v_mul_f32_e32 v99, 0xbfb8aa3b, v92
	v_mul_f32_e32 v101, 0xbfb8aa3b, v94
	v_mul_f32_e32 v92, v92, v93
	v_mul_f32_e32 v93, v94, v95
	v_mul_f32_e32 v94, 0xbfb8aa3b, v90
	v_mul_f32_e32 v95, 0xbfb8aa3b, v88
	v_mul_f32_e32 v96, v96, v97
	v_add_f32_e32 v97, 1.0, v102
	v_exp_f32_e32 v94, v94
	v_exp_f32_e32 v95, v95
	v_rcp_f32_e32 v97, v97
	v_exp_f32_e32 v99, v99
	v_exp_f32_e32 v101, v101
	v_mul_f32_e32 v90, v90, v91
	v_add_f32_e32 v91, 1.0, v94
	v_add_f32_e32 v94, 1.0, v95
	v_mul_f32_e32 v95, 0xbfb8aa3b, v86
	v_mul_f32_e32 v96, v96, v97
	v_add_f32_e32 v97, 1.0, v99
	v_add_f32_e32 v99, 1.0, v101
	v_rcp_f32_e32 v91, v91
	v_rcp_f32_e32 v94, v94
	v_exp_f32_e32 v95, v95
	v_rcp_f32_e32 v99, v99
	v_mul_f32_e32 v88, v88, v89
	v_mul_f32_e32 v90, v90, v91
	v_mul_f32_e32 v91, v88, v94
	v_add_f32_e32 v88, 1.0, v95
	v_rcp_f32_e32 v97, v97
	v_mul_f32_e32 v93, v93, v99
	v_rcp_f32_e32 v94, v88
	v_mov_b32_e32 v88, 0
	v_mov_b32_e32 v89, 0
	v_cvt_pk_fp8_f32 v88, v100, v98
	v_cvt_pk_fp8_f32 v89, v93, v90
	v_mul_f32_e32 v86, v86, v87
	v_mul_f32_e32 v92, v92, v97
	v_mul_f32_e32 v86, v86, v94
	v_cvt_pk_fp8_f32 v88, v96, v92 op_sel:[0,0,1]
	v_cvt_pk_fp8_f32 v89, v91, v86 op_sel:[0,0,1]
	v_mul_f32_e32 v86, 0xbfb8aa3b, v84
	v_or_b32_e32 v104, 32, v122
	v_exp_f32_e32 v90, v86
	v_mad_i64_i32 v[86:87], s[50:51], v104, s81, v[12:13]
	v_lshl_add_u64 v[86:87], v[86:87], 0, v[8:9]
	global_store_dwordx2 v[86:87], v[88:89], off
	v_mul_f32_e32 v87, 0xbfb8aa3b, v82
	v_add_f32_e32 v86, 1.0, v90
	v_exp_f32_e32 v87, v87
	v_rcp_f32_e32 v86, v86
	v_mul_f32_e32 v84, v84, v85
	v_mul_f32_e32 v82, v82, v83
	v_add_f32_e32 v85, 1.0, v87
	v_mul_f32_e32 v84, v84, v86
	v_rcp_f32_e32 v85, v85
	v_mul_f32_e32 v86, 0xbfb8aa3b, v80
	v_exp_f32_e32 v86, v86
	v_mul_f32_e32 v83, 0xbfb8aa3b, v78
	v_mul_f32_e32 v82, v82, v85
	v_mul_f32_e32 v85, 0xbfb8aa3b, v76
	v_mul_f32_e32 v78, v78, v79
	v_mul_f32_e32 v76, v76, v77
	v_mul_f32_e32 v77, 0xbfb8aa3b, v74
	v_mul_f32_e32 v79, 0xbfb8aa3b, v72
	v_mul_f32_e32 v80, v80, v81
	v_add_f32_e32 v81, 1.0, v86
	v_exp_f32_e32 v77, v77
	v_exp_f32_e32 v79, v79
	v_rcp_f32_e32 v81, v81
	v_exp_f32_e32 v83, v83
	v_exp_f32_e32 v85, v85
	v_mul_f32_e32 v74, v74, v75
	v_add_f32_e32 v75, 1.0, v77
	v_add_f32_e32 v77, 1.0, v79
	v_mul_f32_e32 v79, 0xbfb8aa3b, v70
	v_mul_f32_e32 v80, v80, v81
	v_add_f32_e32 v81, 1.0, v83
	v_add_f32_e32 v83, 1.0, v85
	v_rcp_f32_e32 v75, v75
	v_rcp_f32_e32 v77, v77
	v_exp_f32_e32 v79, v79
	v_rcp_f32_e32 v83, v83
	v_mul_f32_e32 v72, v72, v73
	v_mul_f32_e32 v74, v74, v75
	v_mul_f32_e32 v75, v72, v77
	v_add_f32_e32 v72, 1.0, v79
	v_rcp_f32_e32 v81, v81
	v_mul_f32_e32 v76, v76, v83
	v_rcp_f32_e32 v77, v72
	v_mov_b32_e32 v72, 0
	v_mov_b32_e32 v73, 0
	v_cvt_pk_fp8_f32 v72, v84, v82
	v_cvt_pk_fp8_f32 v73, v76, v74
	v_mul_f32_e32 v70, v70, v71
	v_mul_f32_e32 v78, v78, v81
	v_mul_f32_e32 v70, v70, v77
	v_cvt_pk_fp8_f32 v72, v80, v78 op_sel:[0,0,1]
	v_cvt_pk_fp8_f32 v73, v75, v70 op_sel:[0,0,1]
	v_mul_f32_e32 v70, 0xbfb8aa3b, v68
	v_or_b32_e32 v88, 48, v122
	v_exp_f32_e32 v74, v70
	v_mad_i64_i32 v[70:71], s[50:51], v88, s81, v[12:13]
	v_lshl_add_u64 v[70:71], v[70:71], 0, v[8:9]
	global_store_dwordx2 v[70:71], v[72:73], off
	v_mul_f32_e32 v71, 0xbfb8aa3b, v66
	v_add_f32_e32 v70, 1.0, v74
	v_exp_f32_e32 v71, v71
	v_rcp_f32_e32 v70, v70
	v_mul_f32_e32 v68, v68, v69
	v_mul_f32_e32 v66, v66, v67
	v_add_f32_e32 v69, 1.0, v71
	v_mul_f32_e32 v68, v68, v70
	v_rcp_f32_e32 v69, v69
	v_mul_f32_e32 v70, 0xbfb8aa3b, v64
	v_exp_f32_e32 v70, v70
	v_mul_f32_e32 v67, 0xbfb8aa3b, v62
	v_mul_f32_e32 v66, v66, v69
	v_mul_f32_e32 v69, 0xbfb8aa3b, v60
	v_mul_f32_e32 v62, v62, v63
	v_mul_f32_e32 v60, v60, v61
	v_mul_f32_e32 v61, 0xbfb8aa3b, v58
	v_mul_f32_e32 v63, 0xbfb8aa3b, v56
	v_mul_f32_e32 v64, v64, v65
	v_add_f32_e32 v65, 1.0, v70
	v_exp_f32_e32 v61, v61
	v_exp_f32_e32 v63, v63
	v_rcp_f32_e32 v65, v65
	v_exp_f32_e32 v67, v67
	v_exp_f32_e32 v69, v69
	v_mul_f32_e32 v58, v58, v59
	v_add_f32_e32 v59, 1.0, v61
	v_add_f32_e32 v61, 1.0, v63
	v_mul_f32_e32 v63, 0xbfb8aa3b, v54
	v_mul_f32_e32 v64, v64, v65
	v_add_f32_e32 v65, 1.0, v67
	v_add_f32_e32 v67, 1.0, v69
	v_rcp_f32_e32 v59, v59
	v_rcp_f32_e32 v61, v61
	v_exp_f32_e32 v63, v63
	v_rcp_f32_e32 v67, v67
	v_mul_f32_e32 v56, v56, v57
	v_mul_f32_e32 v58, v58, v59
	v_mul_f32_e32 v59, v56, v61
	v_add_f32_e32 v56, 1.0, v63
	v_rcp_f32_e32 v65, v65
	v_mul_f32_e32 v60, v60, v67
	v_rcp_f32_e32 v61, v56
	v_mov_b32_e32 v56, 0
	v_mov_b32_e32 v57, 0
	v_cvt_pk_fp8_f32 v56, v68, v66
	v_cvt_pk_fp8_f32 v57, v60, v58
	v_mul_f32_e32 v54, v54, v55
	v_mul_f32_e32 v62, v62, v65
	v_mul_f32_e32 v54, v54, v61
	v_cvt_pk_fp8_f32 v56, v64, v62 op_sel:[0,0,1]
	v_cvt_pk_fp8_f32 v57, v59, v54 op_sel:[0,0,1]
	v_mul_f32_e32 v54, 0xbfb8aa3b, v52
	v_add_u32_e32 v72, 0x80, v122
	v_exp_f32_e32 v58, v54
	v_mad_i64_i32 v[54:55], s[50:51], v72, s81, v[12:13]
	v_lshl_add_u64 v[54:55], v[54:55], 0, v[8:9]
	global_store_dwordx2 v[54:55], v[56:57], off
	v_mul_f32_e32 v55, 0xbfb8aa3b, v50
	v_add_f32_e32 v54, 1.0, v58
	v_exp_f32_e32 v55, v55
	v_rcp_f32_e32 v54, v54
	v_mul_f32_e32 v52, v52, v53
	v_mul_f32_e32 v50, v50, v51
	v_add_f32_e32 v53, 1.0, v55
	v_mul_f32_e32 v52, v52, v54
	v_rcp_f32_e32 v53, v53
	v_mul_f32_e32 v54, 0xbfb8aa3b, v48
	v_exp_f32_e32 v54, v54
	v_mul_f32_e32 v51, 0xbfb8aa3b, v46
	v_mul_f32_e32 v50, v50, v53
	v_mul_f32_e32 v53, 0xbfb8aa3b, v44
	v_mul_f32_e32 v46, v46, v47
	v_mul_f32_e32 v44, v44, v45
	v_mul_f32_e32 v45, 0xbfb8aa3b, v42
	v_mul_f32_e32 v47, 0xbfb8aa3b, v40
	v_mul_f32_e32 v48, v48, v49
	v_add_f32_e32 v49, 1.0, v54
	v_exp_f32_e32 v45, v45
	v_exp_f32_e32 v47, v47
	v_rcp_f32_e32 v49, v49
	v_exp_f32_e32 v51, v51
	v_exp_f32_e32 v53, v53
	v_mul_f32_e32 v42, v42, v43
	v_add_f32_e32 v43, 1.0, v45
	v_add_f32_e32 v45, 1.0, v47
	v_mul_f32_e32 v47, 0xbfb8aa3b, v38
	v_mul_f32_e32 v48, v48, v49
	v_add_f32_e32 v49, 1.0, v51
	v_add_f32_e32 v51, 1.0, v53
	v_rcp_f32_e32 v43, v43
	v_rcp_f32_e32 v45, v45
	v_exp_f32_e32 v47, v47
	v_rcp_f32_e32 v51, v51
	v_mul_f32_e32 v40, v40, v41
	v_mul_f32_e32 v42, v42, v43
	v_mul_f32_e32 v43, v40, v45
	v_add_f32_e32 v40, 1.0, v47
	v_rcp_f32_e32 v49, v49
	v_mul_f32_e32 v44, v44, v51
	v_rcp_f32_e32 v45, v40
	v_mov_b32_e32 v40, 0
	v_mov_b32_e32 v41, 0
	v_cvt_pk_fp8_f32 v40, v52, v50
	v_cvt_pk_fp8_f32 v41, v44, v42
	v_mul_f32_e32 v38, v38, v39
	v_mul_f32_e32 v46, v46, v49
	v_mul_f32_e32 v38, v38, v45
	v_cvt_pk_fp8_f32 v40, v48, v46 op_sel:[0,0,1]
	v_cvt_pk_fp8_f32 v41, v43, v38 op_sel:[0,0,1]
	v_mul_f32_e32 v38, 0xbfb8aa3b, v36
	v_add_u32_e32 v56, 0x90, v122
	v_exp_f32_e32 v42, v38
	v_mad_i64_i32 v[38:39], s[50:51], v56, s81, v[12:13]
	v_lshl_add_u64 v[38:39], v[38:39], 0, v[8:9]
	global_store_dwordx2 v[38:39], v[40:41], off
	v_mul_f32_e32 v39, 0xbfb8aa3b, v34
	v_add_f32_e32 v38, 1.0, v42
	v_exp_f32_e32 v39, v39
	v_rcp_f32_e32 v38, v38
	v_mul_f32_e32 v36, v36, v37
	v_mul_f32_e32 v34, v34, v35
	v_add_f32_e32 v37, 1.0, v39
	v_mul_f32_e32 v36, v36, v38
	v_rcp_f32_e32 v37, v37
	v_mul_f32_e32 v38, 0xbfb8aa3b, v32
	v_exp_f32_e32 v38, v38
	v_mul_f32_e32 v35, 0xbfb8aa3b, v30
	v_mul_f32_e32 v34, v34, v37
	v_mul_f32_e32 v37, 0xbfb8aa3b, v28
	v_mul_f32_e32 v30, v30, v31
	v_mul_f32_e32 v28, v28, v29
	v_mul_f32_e32 v29, 0xbfb8aa3b, v26
	v_mul_f32_e32 v31, 0xbfb8aa3b, v24
	v_mul_f32_e32 v32, v32, v33
	v_add_f32_e32 v33, 1.0, v38
	v_exp_f32_e32 v29, v29
	v_exp_f32_e32 v31, v31
	v_rcp_f32_e32 v33, v33
	v_exp_f32_e32 v35, v35
	v_exp_f32_e32 v37, v37
	v_mul_f32_e32 v26, v26, v27
	v_add_f32_e32 v27, 1.0, v29
	v_add_f32_e32 v29, 1.0, v31
	v_mul_f32_e32 v31, 0xbfb8aa3b, v22
	v_mul_f32_e32 v32, v32, v33
	v_add_f32_e32 v33, 1.0, v35
	v_add_f32_e32 v35, 1.0, v37
	v_rcp_f32_e32 v27, v27
	v_rcp_f32_e32 v29, v29
	v_exp_f32_e32 v31, v31
	v_rcp_f32_e32 v35, v35
	v_mul_f32_e32 v24, v24, v25
	v_mul_f32_e32 v26, v26, v27
	v_mul_f32_e32 v27, v24, v29
	v_add_f32_e32 v24, 1.0, v31
	v_mul_f32_e32 v28, v28, v35
	v_rcp_f32_e32 v29, v24
	v_mov_b32_e32 v25, 0
	v_rcp_f32_e32 v33, v33
	v_mov_b32_e32 v24, 0
	v_cvt_pk_fp8_f32 v25, v28, v26
	v_cvt_pk_fp8_f32 v24, v36, v34
	v_mul_f32_e32 v22, v22, v23
	v_mul_f32_e32 v22, v22, v29
	v_mul_f32_e32 v30, v30, v33
	v_cvt_pk_fp8_f32 v25, v27, v22 op_sel:[0,0,1]
	v_mul_f32_e32 v22, 0xbfb8aa3b, v20
	v_cvt_pk_fp8_f32 v24, v32, v30 op_sel:[0,0,1]
	v_exp_f32_e32 v26, v22
	v_add_u32_e32 v40, 0xa0, v122
	v_mad_i64_i32 v[22:23], s[50:51], v40, s81, v[12:13]
	v_lshl_add_u64 v[22:23], v[22:23], 0, v[8:9]
	global_store_dwordx2 v[22:23], v[24:25], off
	v_add_f32_e32 v22, 1.0, v26
	v_mul_f32_e32 v23, 0xbfb8aa3b, v16
	v_rcp_f32_e32 v22, v22
	v_exp_f32_e32 v23, v23
	v_mul_f32_e32 v20, v20, v21
	v_mul_f32_e32 v16, v16, v17
	v_mul_f32_e32 v20, v20, v22
	v_add_f32_e32 v21, 1.0, v23
	v_mul_f32_e32 v22, 0xbfb8aa3b, v14
	v_rcp_f32_e32 v21, v21
	v_exp_f32_e32 v22, v22
	v_mul_f32_e32 v14, v14, v15
	v_mul_f32_e32 v17, 0xbfb8aa3b, v6
	v_mul_f32_e32 v16, v16, v21
	v_add_f32_e32 v15, 1.0, v22
	v_mul_f32_e32 v21, 0xbfb8aa3b, v18
	v_rcp_f32_e32 v15, v15
	v_exp_f32_e32 v17, v17
	v_exp_f32_e32 v21, v21
	v_mul_f32_e32 v6, v6, v7
	v_mul_f32_e32 v14, v14, v15
	v_add_f32_e32 v15, 1.0, v17
	v_add_f32_e32 v17, 1.0, v21
	v_rcp_f32_e32 v15, v15
	v_rcp_f32_e32 v17, v17
	v_mul_f32_e32 v7, v18, v19
	v_add_u32_e32 v24, 0xb0, v122
	v_mul_f32_e32 v6, v6, v15
	v_mul_f32_e32 v7, v7, v17
	v_mul_f32_e32 v15, 0xbfb8aa3b, v10
	v_mul_f32_e32 v17, 0xbfb8aa3b, v4
	v_exp_f32_e32 v15, v15
	v_exp_f32_e32 v17, v17
	v_mul_f32_e32 v10, v10, v11
	v_mul_f32_e32 v4, v4, v5
	v_add_f32_e32 v11, 1.0, v15
	v_add_f32_e32 v15, 1.0, v17
	v_mul_f32_e32 v17, 0xbfb8aa3b, v2
	v_rcp_f32_e32 v11, v11
	v_rcp_f32_e32 v15, v15
	v_exp_f32_e32 v17, v17
	v_mov_b32_e32 v5, 0
	v_mul_f32_e32 v10, v10, v11
	v_mul_f32_e32 v11, v4, v15
	v_add_f32_e32 v4, 1.0, v17
	v_rcp_f32_e32 v15, v4
	v_mov_b32_e32 v4, 0
	v_cvt_pk_fp8_f32 v4, v20, v16
	v_cvt_pk_fp8_f32 v5, v7, v10
	v_mul_f32_e32 v2, v2, v3
	v_mul_f32_e32 v2, v2, v15
	v_cvt_pk_fp8_f32 v4, v14, v6 op_sel:[0,0,1]
	v_cvt_pk_fp8_f32 v5, v11, v2 op_sel:[0,0,1]
	v_mad_i64_i32 v[2:3], s[50:51], v24, s81, v[12:13]
	v_lshl_add_u64 v[2:3], v[2:3], 0, v[8:9]
	s_andn2_b64 vcc, exec, s[42:43]
	s_mov_b64 s[42:43], -1
	global_store_dwordx2 v[2:3], v[4:5], off
	s_cbranch_vccnz .LBB0_1716
	s_andn2_b64 vcc, exec, s[22:23]
	s_cbranch_vccnz .LBB0_1715
	s_barrier
	s_branch .LBB0_1715
